# speedup vs baseline: 1.0258x; 1.0101x over previous
.LBB2_101:
	s_or_b64 exec, exec, s[40:41]
	s_load_dwordx2 s[2:3], s[0:1], 0x90
	s_load_dwordx2 s[4:5], s[0:1], 0x0
	s_load_dwordx2 s[6:7], s[0:1], 0x30
	v_lshlrev_b32_e32 v132, 15, v66
	v_mov_b32_e32 v133, 0
	s_waitcnt lgkmcnt(0)
	v_lshl_add_u64 v[26:27], s[6:7], 0, v[132:133]
	v_lshlrev_b32_e32 v132, 4, v146
	v_lshl_add_u64 v[66:67], v[26:27], 0, v[132:133]
	s_movk_i32 s9, 0x1000
	v_add_co_u32_e32 v68, vcc, s9, v66
	s_movk_i32 s11, 0x2000
	s_nop 0
	v_addc_co_u32_e32 v69, vcc, 0, v67, vcc
	v_add_co_u32_e32 v70, vcc, s11, v66
	global_load_dwordx4 v[86:89], v[66:67], off
	s_nop 0
	v_addc_co_u32_e32 v71, vcc, 0, v67, vcc
	global_load_dwordx4 v[90:93], v[70:71], off offset:-4096
	s_movk_i32 s12, 0x3000
	v_add_co_u32_e32 v72, vcc, s12, v66
	s_movk_i32 s8, 0x4000
	s_nop 0
	v_addc_co_u32_e32 v73, vcc, 0, v67, vcc
	v_add_co_u32_e32 v74, vcc, s8, v66
	global_load_dwordx4 v[94:97], v[70:71], off
	s_waitcnt vmcnt(4)
	v_addc_co_u32_e32 v75, vcc, 0, v67, vcc
	global_load_dwordx4 v[98:101], v[74:75], off offset:-4096
	s_movk_i32 s10, 0x5000
	v_add_co_u32_e32 v76, vcc, s10, v66
	s_movk_i32 s7, 0x6000
	s_nop 0
	v_addc_co_u32_e32 v77, vcc, 0, v67, vcc
	v_add_co_u32_e32 v78, vcc, s7, v66
	global_load_dwordx4 v[102:105], v[74:75], off
	s_nop 0
	v_addc_co_u32_e32 v79, vcc, 0, v67, vcc
	global_load_dwordx4 v[110:113], v[78:79], off
	global_load_dwordx4 v[106:109], v[78:79], off offset:-4096
	s_movk_i32 s6, 0x7000
	v_add_co_u32_e32 v80, vcc, s6, v66
	s_movk_i32 s0, 0x110
	s_nop 0
	v_addc_co_u32_e32 v81, vcc, 0, v67, vcc
	global_load_dwordx4 v[114:117], v[80:81], off
	global_load_dwordx4 v[58:61], v[66:67], off offset:1024
	global_load_dwordx4 v[62:65], v[68:69], off offset:1024
	global_load_dwordx4 v[54:57], v[70:71], off offset:1024
	global_load_dwordx4 v[50:53], v[72:73], off offset:1024
	global_load_dwordx4 v[46:49], v[74:75], off offset:1024
	global_load_dwordx4 v[42:45], v[76:77], off offset:1024
	global_load_dwordx4 v[34:37], v[78:79], off offset:1024
	global_load_dwordx4 v[26:29], v[80:81], off offset:1024
	v_mad_u32_u24 v85, v131, s0, v130
	v_add_u32_e32 v151, v85, v147
	ds_read_b128 v[38:41], v147 offset:17408
	s_waitcnt vmcnt(16)
	ds_read_b128 v[30:33], v147 offset:17472
	ds_read_b128 v[118:121], v151
	ds_read_b128 v[122:125], v151 offset:4352
	ds_read_b128 v[164:167], v151 offset:4416
	s_waitcnt vmcnt(15) lgkmcnt(2)
	v_mfma_f32_16x16x32_f16 v[126:129], v[86:89], v[118:121], v[38:41]
	s_waitcnt lgkmcnt(1)
	v_mfma_f32_16x16x32_f16 v[86:89], v[86:89], v[122:125], v[38:41]
	s_waitcnt vmcnt(14)
	v_mfma_f32_16x16x32_f16 v[134:137], v[90:93], v[118:121], v[30:33]
	v_mfma_f32_16x16x32_f16 v[90:93], v[90:93], v[122:125], v[30:33]
	global_load_dwordx4 v[38:41], v[66:67], off offset:2048
	s_nop 1
	global_load_dwordx4 v[30:33], v[68:69], off offset:2048
	ds_read_b128 v[22:25], v147 offset:17536
	ds_read_b128 v[18:21], v147 offset:17600
	s_waitcnt vmcnt(15) lgkmcnt(1)
	v_mfma_f32_16x16x32_f16 v[138:141], v[94:97], v[118:121], v[22:25]
	v_mfma_f32_16x16x32_f16 v[94:97], v[94:97], v[122:125], v[22:25]
	s_waitcnt vmcnt(14) lgkmcnt(0)
	v_mfma_f32_16x16x32_f16 v[142:145], v[98:101], v[118:121], v[18:21]
	v_mfma_f32_16x16x32_f16 v[98:101], v[98:101], v[122:125], v[18:21]
	global_load_dwordx4 v[22:25], v[70:71], off offset:2048
	s_nop 1
	global_load_dwordx4 v[18:21], v[72:73], off offset:2048
	ds_read_b128 v[6:9], v147 offset:17792
	s_waitcnt vmcnt(14) lgkmcnt(0)
	v_mfma_f32_16x16x32_f16 v[160:163], v[110:113], v[118:121], v[6:9]
	v_mfma_f32_16x16x32_f16 v[110:113], v[110:113], v[122:125], v[6:9]
	s_nop 2
	global_load_dwordx4 v[6:9], v[78:79], off offset:2048
	ds_read_b128 v[10:13], v147 offset:17728
	s_waitcnt vmcnt(14) lgkmcnt(0)
	v_mfma_f32_16x16x32_f16 v[156:159], v[106:109], v[118:121], v[10:13]
	v_mfma_f32_16x16x32_f16 v[106:109], v[106:109], v[122:125], v[10:13]
	s_nop 2
	global_load_dwordx4 v[10:13], v[76:77], off offset:2048
	ds_read_b128 v[14:17], v147 offset:17664
	s_waitcnt lgkmcnt(0)
	v_mfma_f32_16x16x32_f16 v[152:155], v[102:105], v[118:121], v[14:17]
	ds_read_b128 v[2:5], v147 offset:17856
	s_waitcnt vmcnt(14) lgkmcnt(0)
	v_mfma_f32_16x16x32_f16 v[118:121], v[114:117], v[118:121], v[2:5]
	v_mfma_f32_16x16x32_f16 v[114:117], v[114:117], v[122:125], v[2:5]
	s_nop 2
	global_load_dwordx4 v[2:5], v[80:81], off offset:2048
	v_mfma_f32_16x16x32_f16 v[102:105], v[102:105], v[122:125], v[14:17]
	ds_read_b128 v[122:125], v151 offset:64
	s_nop 1
	global_load_dwordx4 v[14:17], v[74:75], off offset:2048
	s_waitcnt vmcnt(15) lgkmcnt(0)
	v_mfma_f32_16x16x32_f16 v[126:129], v[58:61], v[122:125], v[126:129]
	v_mfma_f32_16x16x32_f16 v[58:61], v[58:61], v[164:167], v[86:89]
	s_waitcnt vmcnt(14)
	v_mfma_f32_16x16x32_f16 v[86:89], v[62:65], v[122:125], v[134:137]
	v_mfma_f32_16x16x32_f16 v[62:65], v[62:65], v[164:167], v[90:93]
	s_nop 1
	global_load_dwordx4 v[134:137], v[70:71], off offset:3072
	s_nop 0
	global_load_dwordx4 v[70:73], v[72:73], off offset:3072
	s_waitcnt vmcnt(15)
	v_mfma_f32_16x16x32_f16 v[90:93], v[54:57], v[122:125], v[138:141]
	v_mfma_f32_16x16x32_f16 v[54:57], v[54:57], v[164:167], v[94:97]
	s_nop 1
	global_load_dwordx4 v[138:141], v[74:75], off offset:3072
	s_nop 0
	global_load_dwordx4 v[74:77], v[76:77], off offset:3072
	s_waitcnt vmcnt(16)
	v_mfma_f32_16x16x32_f16 v[94:97], v[50:53], v[122:125], v[142:145]
	v_mfma_f32_16x16x32_f16 v[50:53], v[50:53], v[164:167], v[98:101]
	s_nop 1
	global_load_dwordx4 v[142:145], v[78:79], off offset:3072
	s_nop 0
	global_load_dwordx4 v[78:81], v[80:81], off offset:3072
	s_waitcnt vmcnt(17)
	v_mfma_f32_16x16x32_f16 v[98:101], v[46:49], v[122:125], v[152:155]
	v_mfma_f32_16x16x32_f16 v[46:49], v[46:49], v[164:167], v[102:105]
	s_waitcnt vmcnt(16)
	v_mfma_f32_16x16x32_f16 v[102:105], v[42:45], v[122:125], v[156:159]
	v_mfma_f32_16x16x32_f16 v[42:45], v[42:45], v[164:167], v[106:109]
	s_waitcnt vmcnt(15)
	v_mfma_f32_16x16x32_f16 v[106:109], v[34:37], v[122:125], v[160:163]
	v_mfma_f32_16x16x32_f16 v[34:37], v[34:37], v[164:167], v[110:113]
	s_waitcnt vmcnt(14)
	v_mfma_f32_16x16x32_f16 v[110:113], v[26:29], v[122:125], v[118:121]
	ds_read_b128 v[122:125], v151 offset:4480
	v_mfma_f32_16x16x32_f16 v[26:29], v[26:29], v[164:167], v[114:117]
	s_nop 0
	ds_read_b128 v[118:121], v151 offset:128
	s_nop 0
	global_load_dwordx4 v[114:117], v[66:67], off offset:3072
	s_nop 0
	global_load_dwordx4 v[66:69], v[68:69], off offset:3072
	s_waitcnt vmcnt(15) lgkmcnt(0)
	v_mfma_f32_16x16x32_f16 v[126:129], v[38:41], v[118:121], v[126:129]
	v_mfma_f32_16x16x32_f16 v[38:41], v[38:41], v[122:125], v[58:61]
	s_waitcnt vmcnt(14)
	v_mfma_f32_16x16x32_f16 v[58:61], v[30:33], v[118:121], v[86:89]
	s_waitcnt vmcnt(13)
	v_mfma_f32_16x16x32_f16 v[86:89], v[22:25], v[118:121], v[90:93]
	v_mfma_f32_16x16x32_f16 v[22:25], v[22:25], v[122:125], v[54:57]
	s_nop 1
	ds_read_b128 v[90:93], v151 offset:192
	s_waitcnt vmcnt(12)
	v_mfma_f32_16x16x32_f16 v[54:57], v[18:21], v[118:121], v[94:97]
	s_nop 2
	ds_read_b128 v[94:97], v151 offset:4544
	v_mfma_f32_16x16x32_f16 v[62:65], v[30:33], v[122:125], v[62:65]
	v_mfma_f32_16x16x32_f16 v[18:21], v[18:21], v[122:125], v[50:53]
	s_waitcnt vmcnt(8)
	v_mfma_f32_16x16x32_f16 v[50:53], v[14:17], v[118:121], v[98:101]
	v_mfma_f32_16x16x32_f16 v[14:17], v[14:17], v[122:125], v[46:49]
	v_mfma_f32_16x16x32_f16 v[46:49], v[10:13], v[118:121], v[102:105]
	v_mfma_f32_16x16x32_f16 v[10:13], v[10:13], v[122:125], v[42:45]
	v_mfma_f32_16x16x32_f16 v[42:45], v[6:9], v[118:121], v[106:109]
	v_mfma_f32_16x16x32_f16 v[6:9], v[6:9], v[122:125], v[34:37]
	v_mfma_f32_16x16x32_f16 v[34:37], v[2:5], v[118:121], v[110:113]
	v_mfma_f32_16x16x32_f16 v[2:5], v[2:5], v[122:125], v[26:29]
	s_waitcnt vmcnt(1) lgkmcnt(0)
	v_mfma_f32_16x16x32_f16 v[30:33], v[114:117], v[94:97], v[38:41]
	s_waitcnt vmcnt(0)
	v_mfma_f32_16x16x32_f16 v[26:29], v[66:69], v[94:97], v[62:65]
	v_mfma_f32_16x16x32_f16 v[22:25], v[134:137], v[94:97], v[22:25]
	v_mfma_f32_16x16x32_f16 v[18:21], v[70:73], v[94:97], v[18:21]
	v_mfma_f32_16x16x32_f16 v[14:17], v[138:141], v[94:97], v[14:17]
	v_mfma_f32_16x16x32_f16 v[10:13], v[74:77], v[94:97], v[10:13]
	v_mfma_f32_16x16x32_f16 v[6:9], v[142:145], v[94:97], v[6:9]
	v_mfma_f32_16x16x32_f16 v[2:5], v[78:81], v[94:97], v[2:5]
	v_mfma_f32_16x16x32_f16 v[126:129], v[114:117], v[90:93], v[126:129]
	v_mfma_f32_16x16x32_f16 v[122:125], v[66:69], v[90:93], v[58:61]
	v_mfma_f32_16x16x32_f16 v[118:121], v[134:137], v[90:93], v[86:89]
	v_mfma_f32_16x16x32_f16 v[114:117], v[70:73], v[90:93], v[54:57]
	v_mfma_f32_16x16x32_f16 v[106:109], v[138:141], v[90:93], v[50:53]
	v_mfma_f32_16x16x32_f16 v[110:113], v[74:77], v[90:93], v[46:49]
	v_mfma_f32_16x16x32_f16 v[102:105], v[142:145], v[90:93], v[42:45]
	v_mfma_f32_16x16x32_f16 v[98:101], v[78:81], v[90:93], v[34:37]
	s_nop 2
	v_xor_b32_e32 v34, 16, v83
	v_add_u32_e32 v35, 64, v84
	v_cmp_lt_i32_e32 vcc, v34, v35
	v_mov_b32_e32 v36, v127
	v_mov_b32_e32 v37, v123
	v_cndmask_b32_e32 v34, v83, v34, vcc
	v_lshlrev_b32_e32 v149, 2, v34
	v_xor_b32_e32 v34, 32, v83
	v_cmp_lt_i32_e32 vcc, v34, v35
	v_mov_b32_e32 v35, v122
	v_mov_b32_e32 v38, v129
	v_cndmask_b32_e32 v34, v83, v34, vcc
	v_lshlrev_b32_e32 v148, 2, v34
	v_mov_b32_e32 v34, v126
	v_pk_add_f32 v[34:35], v[34:35], v[36:37]
	v_mov_b32_e32 v36, v128
	v_mov_b32_e32 v37, v124
	v_mov_b32_e32 v39, v125
	v_pk_add_f32 v[36:37], v[36:37], v[38:39]
	v_mov_b32_e32 v38, v118
	v_pk_add_f32 v[34:35], v[34:35], v[36:37]
	v_mov_b32_e32 v36, v119
	v_mov_b32_e32 v37, v120
	v_mov_b32_e32 v39, v121
	v_pk_add_f32 v[36:37], v[36:37], v[38:39]
	v_add_f32_e32 v34, 0, v34
	v_pk_add_f32 v[36:37], v[36:37], v[36:37] op_sel:[0,1] op_sel_hi:[1,0]
	v_add_f32_e32 v34, v34, v35
	v_add_f32_e32 v38, v114, v115
	v_add_f32_e32 v40, v116, v117
	v_mov_b32_e32 v35, v106
	v_mov_b32_e32 v37, v107
	v_mov_b32_e32 v39, v108
	v_mov_b32_e32 v41, v109
	v_pk_add_f32 v[34:35], v[34:35], v[36:37]
	v_pk_add_f32 v[36:37], v[38:39], v[40:41]
	v_mov_b32_e32 v38, v110
	v_pk_add_f32 v[34:35], v[34:35], v[36:37]
	v_mov_b32_e32 v36, v111
	v_mov_b32_e32 v37, v112
	v_mov_b32_e32 v39, v113
	v_pk_add_f32 v[36:37], v[36:37], v[38:39]
	v_pk_add_f32 v[34:35], v[34:35], v[34:35] op_sel:[0,1] op_sel_hi:[1,0]
	v_pk_add_f32 v[36:37], v[36:37], v[36:37] op_sel:[0,1] op_sel_hi:[1,0]
	v_add_f32_e32 v38, v102, v103
	v_add_f32_e32 v40, v104, v105
	v_mov_b32_e32 v35, v98
	v_mov_b32_e32 v37, v99
	v_mov_b32_e32 v39, v100
	v_mov_b32_e32 v41, v101
	v_pk_add_f32 v[34:35], v[34:35], v[36:37]
	v_pk_add_f32 v[36:37], v[38:39], v[40:41]
	v_mov_b32_e32 v38, v31
	v_pk_add_f32 v[34:35], v[34:35], v[36:37]
	v_mov_b32_e32 v36, v30
	v_mov_b32_e32 v37, v26
	v_mov_b32_e32 v39, v27
	v_pk_add_f32 v[36:37], v[36:37], v[38:39]
	v_mov_b32_e32 v38, v32
	v_mov_b32_e32 v39, v28
	v_mov_b32_e32 v40, v33
	v_mov_b32_e32 v41, v29
	v_pk_add_f32 v[38:39], v[38:39], v[40:41]
	v_mov_b32_e32 v40, v22
	v_pk_add_f32 v[36:37], v[36:37], v[38:39]
	v_mov_b32_e32 v38, v23
	v_mov_b32_e32 v39, v24
	v_mov_b32_e32 v41, v25
	v_pk_add_f32 v[38:39], v[38:39], v[40:41]
	v_add_f32_e32 v36, 0, v36
	v_pk_add_f32 v[38:39], v[38:39], v[38:39] op_sel:[0,1] op_sel_hi:[1,0]
	v_add_f32_e32 v36, v36, v37
	v_add_f32_e32 v40, v18, v19
	v_add_f32_e32 v42, v20, v21
	v_mov_b32_e32 v37, v14
	v_mov_b32_e32 v39, v15
	v_mov_b32_e32 v41, v16
	v_mov_b32_e32 v43, v17
	v_pk_add_f32 v[36:37], v[36:37], v[38:39]
	v_pk_add_f32 v[38:39], v[40:41], v[42:43]
	v_mov_b32_e32 v40, v10
	v_pk_add_f32 v[36:37], v[36:37], v[38:39]
	v_mov_b32_e32 v38, v11
	v_mov_b32_e32 v39, v12
	v_mov_b32_e32 v41, v13
	v_pk_add_f32 v[38:39], v[38:39], v[40:41]
	v_pk_add_f32 v[36:37], v[36:37], v[36:37] op_sel:[0,1] op_sel_hi:[1,0]
	v_pk_add_f32 v[38:39], v[38:39], v[38:39] op_sel:[0,1] op_sel_hi:[1,0]
	v_add_f32_e32 v40, v6, v7
	v_add_f32_e32 v42, v8, v9
	v_mov_b32_e32 v37, v2
	v_mov_b32_e32 v39, v3
	v_mov_b32_e32 v41, v4
	v_mov_b32_e32 v43, v5
	v_pk_add_f32 v[36:37], v[36:37], v[38:39]
	v_pk_add_f32 v[38:39], v[40:41], v[42:43]
	s_brev_b32 s0, 60
	v_pk_add_f32 v[36:37], v[36:37], v[38:39]
	v_mov_b32_e32 v39, v34
	v_mov_b32_e32 v38, v36
	v_mov_b32_e32 v34, v37
	v_pk_add_f32 v[34:35], v[38:39], v[34:35]
	ds_bpermute_b32 v37, v149, v35
	ds_bpermute_b32 v36, v149, v34
	v_mov_b32_e32 v165, v126
	v_mov_b32_e32 v164, v30
	v_lshlrev_b32_e32 v150, 4, v82
	ds_read_b128 v[38:41], v150 offset:18880
	s_waitcnt lgkmcnt(1)
	v_pk_add_f32 v[134:135], v[34:35], v[36:37]
	ds_bpermute_b32 v137, v148, v135
	ds_bpermute_b32 v136, v148, v134
	ds_read_b128 v[34:37], v150 offset:18368
	ds_read_b128 v[42:45], v150 offset:18304
	ds_read_b128 v[46:49], v150 offset:18816
	ds_read_b128 v[90:93], v150 offset:17920
	s_waitcnt lgkmcnt(4)
	v_pk_add_f32 v[144:145], v[134:135], v[136:137]
	ds_read_b128 v[94:97], v150 offset:18432
	v_pk_mul_f32 v[134:135], v[144:145], s[0:1] op_sel_hi:[1,0]
	v_pk_fma_f32 v[164:165], v[144:145], s[0:1], v[164:165] op_sel_hi:[1,0,1] neg_lo:[1,0,0] neg_hi:[1,0,0]
	v_sub_f32_e32 v163, v126, v135
	v_mov_b32_e32 v126, v31
	v_sub_f32_e32 v162, v127, v135
	v_pk_fma_f32 v[126:127], v[144:145], s[0:1], v[126:127] op_sel_hi:[1,0,1] neg_lo:[1,0,0] neg_hi:[1,0,0]
	v_sub_f32_e32 v161, v128, v135
	v_pk_mul_f32 v[126:127], v[126:127], v[126:127]
	v_sub_f32_e32 v159, v122, v135
	v_pk_fma_f32 v[126:127], v[164:165], v[164:165], v[126:127]
	v_mov_b32_e32 v164, v32
	v_mov_b32_e32 v165, v128
	v_pk_fma_f32 v[164:165], v[144:145], s[0:1], v[164:165] op_sel_hi:[1,0,1] neg_lo:[1,0,0] neg_hi:[1,0,0]
	v_mov_b32_e32 v128, v33
	v_pk_fma_f32 v[126:127], v[164:165], v[164:165], v[126:127]
	v_pk_fma_f32 v[164:165], v[144:145], s[0:1], v[128:129] op_sel_hi:[1,0,1] neg_lo:[1,0,0] neg_hi:[1,0,0]
	v_sub_f32_e32 v158, v123, v135
	v_pk_fma_f32 v[126:127], v[164:165], v[164:165], v[126:127]
	v_mov_b32_e32 v164, v26
	v_mov_b32_e32 v165, v122
	v_pk_fma_f32 v[164:165], v[144:145], s[0:1], v[164:165] op_sel_hi:[1,0,1] neg_lo:[1,0,0] neg_hi:[1,0,0]
	v_mov_b32_e32 v122, v27
	v_pk_fma_f32 v[126:127], v[164:165], v[164:165], v[126:127]
	v_pk_fma_f32 v[122:123], v[144:145], s[0:1], v[122:123] op_sel_hi:[1,0,1] neg_lo:[1,0,0] neg_hi:[1,0,0]
	v_sub_f32_e32 v156, v124, v135
	v_pk_fma_f32 v[122:123], v[122:123], v[122:123], v[126:127]
	v_mov_b32_e32 v126, v28
	v_mov_b32_e32 v127, v124
	v_pk_fma_f32 v[126:127], v[144:145], s[0:1], v[126:127] op_sel_hi:[1,0,1] neg_lo:[1,0,0] neg_hi:[1,0,0]
	v_mov_b32_e32 v124, v29
	v_pk_fma_f32 v[122:123], v[126:127], v[126:127], v[122:123]
	v_pk_fma_f32 v[164:165], v[144:145], s[0:1], v[124:125] op_sel_hi:[1,0,1] neg_lo:[1,0,0] neg_hi:[1,0,0]
	v_sub_f32_e32 v153, v118, v135
	v_pk_fma_f32 v[122:123], v[164:165], v[164:165], v[122:123]
	v_mov_b32_e32 v164, v22
	v_mov_b32_e32 v165, v118
	v_pk_fma_f32 v[164:165], v[144:145], s[0:1], v[164:165] op_sel_hi:[1,0,1] neg_lo:[1,0,0] neg_hi:[1,0,0]
	v_mov_b32_e32 v118, v23
	v_sub_f32_e32 v157, v119, v135
	v_pk_fma_f32 v[122:123], v[164:165], v[164:165], v[122:123]
	v_pk_fma_f32 v[118:119], v[144:145], s[0:1], v[118:119] op_sel_hi:[1,0,1] neg_lo:[1,0,0] neg_hi:[1,0,0]
	v_sub_f32_e32 v155, v120, v135
	v_pk_fma_f32 v[118:119], v[118:119], v[118:119], v[122:123]
	v_mov_b32_e32 v122, v24
	v_mov_b32_e32 v123, v120
	v_pk_fma_f32 v[122:123], v[144:145], s[0:1], v[122:123] op_sel_hi:[1,0,1] neg_lo:[1,0,0] neg_hi:[1,0,0]
	v_mov_b32_e32 v120, v25
	v_sub_f32_e32 v160, v129, v135
	v_sub_f32_e32 v129, v121, v135
	v_pk_fma_f32 v[164:165], v[122:123], v[122:123], v[118:119]
	v_pk_fma_f32 v[120:121], v[144:145], s[0:1], v[120:121] op_sel_hi:[1,0,1] neg_lo:[1,0,0] neg_hi:[1,0,0]
	v_sub_f32_e32 v128, v114, v135
	v_pk_fma_f32 v[120:121], v[120:121], v[120:121], v[164:165]
	v_mov_b32_e32 v164, v18
	v_mov_b32_e32 v165, v114
	v_pk_fma_f32 v[164:165], v[144:145], s[0:1], v[164:165] op_sel_hi:[1,0,1] neg_lo:[1,0,0] neg_hi:[1,0,0]
	v_mov_b32_e32 v114, v19
	v_sub_f32_e32 v127, v115, v135
	v_pk_fma_f32 v[120:121], v[164:165], v[164:165], v[120:121]
	v_pk_fma_f32 v[114:115], v[144:145], s[0:1], v[114:115] op_sel_hi:[1,0,1] neg_lo:[1,0,0] neg_hi:[1,0,0]
	v_sub_f32_e32 v126, v116, v135
	v_pk_fma_f32 v[114:115], v[114:115], v[114:115], v[120:121]
	v_mov_b32_e32 v120, v20
	v_mov_b32_e32 v121, v116
	v_pk_fma_f32 v[120:121], v[144:145], s[0:1], v[120:121] op_sel_hi:[1,0,1] neg_lo:[1,0,0] neg_hi:[1,0,0]
	v_mov_b32_e32 v116, v21
	v_sub_f32_e32 v154, v125, v135
	v_sub_f32_e32 v125, v117, v135
	v_pk_fma_f32 v[114:115], v[120:121], v[120:121], v[114:115]
	v_pk_fma_f32 v[116:117], v[144:145], s[0:1], v[116:117] op_sel_hi:[1,0,1] neg_lo:[1,0,0] neg_hi:[1,0,0]
	v_sub_f32_e32 v124, v106, v135
	v_pk_fma_f32 v[114:115], v[116:117], v[116:117], v[114:115]
	v_mov_b32_e32 v116, v14
	v_mov_b32_e32 v117, v106
	v_pk_fma_f32 v[116:117], v[144:145], s[0:1], v[116:117] op_sel_hi:[1,0,1] neg_lo:[1,0,0] neg_hi:[1,0,0]
	v_mov_b32_e32 v106, v15
	v_sub_f32_e32 v123, v107, v135
	v_pk_fma_f32 v[114:115], v[116:117], v[116:117], v[114:115]
	v_pk_fma_f32 v[106:107], v[144:145], s[0:1], v[106:107] op_sel_hi:[1,0,1] neg_lo:[1,0,0] neg_hi:[1,0,0]
	v_sub_f32_e32 v122, v108, v135
	v_pk_fma_f32 v[106:107], v[106:107], v[106:107], v[114:115]
	v_mov_b32_e32 v114, v16
	v_mov_b32_e32 v115, v108
	v_pk_fma_f32 v[114:115], v[144:145], s[0:1], v[114:115] op_sel_hi:[1,0,1] neg_lo:[1,0,0] neg_hi:[1,0,0]
	v_mov_b32_e32 v108, v17
	v_pk_fma_f32 v[106:107], v[114:115], v[114:115], v[106:107]
	v_pk_fma_f32 v[114:115], v[144:145], s[0:1], v[108:109] op_sel_hi:[1,0,1] neg_lo:[1,0,0] neg_hi:[1,0,0]
	v_sub_f32_e32 v119, v110, v135
	v_pk_fma_f32 v[106:107], v[114:115], v[114:115], v[106:107]
	v_mov_b32_e32 v114, v10
	v_mov_b32_e32 v115, v110
	v_pk_fma_f32 v[114:115], v[144:145], s[0:1], v[114:115] op_sel_hi:[1,0,1] neg_lo:[1,0,0] neg_hi:[1,0,0]
	v_mov_b32_e32 v110, v11
	v_pk_fma_f32 v[106:107], v[114:115], v[114:115], v[106:107]
	v_pk_fma_f32 v[114:115], v[144:145], s[0:1], v[110:111] op_sel_hi:[1,0,1] neg_lo:[1,0,0] neg_hi:[1,0,0]
	v_sub_f32_e32 v118, v112, v135
	v_pk_fma_f32 v[106:107], v[114:115], v[114:115], v[106:107]
	v_mov_b32_e32 v114, v12
	v_mov_b32_e32 v115, v112
	v_pk_fma_f32 v[114:115], v[144:145], s[0:1], v[114:115] op_sel_hi:[1,0,1] neg_lo:[1,0,0] neg_hi:[1,0,0]
	v_mov_b32_e32 v112, v13
	v_pk_fma_f32 v[106:107], v[114:115], v[114:115], v[106:107]
	v_pk_fma_f32 v[114:115], v[144:145], s[0:1], v[112:113] op_sel_hi:[1,0,1] neg_lo:[1,0,0] neg_hi:[1,0,0]
	v_pk_add_f32 v[136:137], v[102:103], v[134:135] op_sel:[0,1] neg_lo:[0,1] neg_hi:[0,1]
	v_pk_fma_f32 v[106:107], v[114:115], v[114:115], v[106:107]
	v_pk_add_f32 v[114:115], v[6:7], v[134:135] op_sel_hi:[1,0] neg_lo:[0,1] neg_hi:[0,1]
	v_pk_mul_f32 v[142:143], v[136:137], v[136:137]
	v_pk_mul_f32 v[114:115], v[114:115], v[114:115]
	v_mov_b32_e32 v117, v142
	v_mov_b32_e32 v116, v114
	v_pk_add_f32 v[136:137], v[104:105], v[134:135] op_sel:[0,1] neg_lo:[0,1] neg_hi:[0,1]
	v_pk_add_f32 v[106:107], v[116:117], v[106:107]
	v_pk_add_f32 v[116:117], v[8:9], v[134:135] op_sel_hi:[1,0] neg_lo:[0,1] neg_hi:[0,1]
	v_pk_mul_f32 v[140:141], v[136:137], v[136:137]
	v_pk_mul_f32 v[116:117], v[116:117], v[116:117]
	v_mov_b32_e32 v142, v115
	v_pk_add_f32 v[136:137], v[98:99], v[134:135] op_sel:[0,1] neg_lo:[0,1] neg_hi:[0,1]
	v_pk_add_f32 v[120:121], v[2:3], v[134:135] op_sel_hi:[1,0] neg_lo:[0,1] neg_hi:[0,1]
	v_pk_add_f32 v[106:107], v[142:143], v[106:107]
	v_mov_b32_e32 v114, v116
	v_mov_b32_e32 v115, v140
	v_pk_mul_f32 v[138:139], v[136:137], v[136:137]
	v_pk_mul_f32 v[120:121], v[120:121], v[120:121]
	v_pk_add_f32 v[106:107], v[114:115], v[106:107]
	v_mov_b32_e32 v140, v117
	v_pk_add_f32 v[136:137], v[100:101], v[134:135] op_sel:[0,1] neg_lo:[0,1] neg_hi:[0,1]
	v_pk_add_f32 v[144:145], v[4:5], v[134:135] op_sel_hi:[1,0] neg_lo:[0,1] neg_hi:[0,1]
	v_pk_add_f32 v[106:107], v[140:141], v[106:107]
	v_mov_b32_e32 v114, v120
	v_mov_b32_e32 v115, v138
	v_pk_mul_f32 v[136:137], v[136:137], v[136:137]
	v_pk_mul_f32 v[144:145], v[144:145], v[144:145]
	v_pk_add_f32 v[106:107], v[114:115], v[106:107]
	v_mov_b32_e32 v138, v121
	v_pk_add_f32 v[106:107], v[138:139], v[106:107]
	v_mov_b32_e32 v114, v144
	v_mov_b32_e32 v115, v136
	v_pk_add_f32 v[106:107], v[114:115], v[106:107]
	v_mov_b32_e32 v136, v145
	v_pk_add_f32 v[106:107], v[136:137], v[106:107]
	ds_bpermute_b32 v115, v149, v107
	ds_bpermute_b32 v114, v149, v106
	v_sub_f32_e32 v121, v109, v135
	v_sub_f32_e32 v116, v102, v135
	v_sub_f32_e32 v112, v98, v135
	v_sub_f32_e32 v120, v111, v135
	s_waitcnt lgkmcnt(0)
	v_pk_add_f32 v[106:107], v[106:107], v[114:115]
	ds_bpermute_b32 v109, v148, v107
	ds_bpermute_b32 v108, v148, v106
	v_sub_f32_e32 v115, v103, v135
	v_sub_f32_e32 v111, v99, v135
	v_sub_f32_e32 v114, v104, v135
	v_lshl_add_u32 v152, v82, 3, v85
	s_waitcnt lgkmcnt(0)
	v_pk_add_f32 v[102:103], v[106:107], v[108:109]
	v_mov_b32_e32 v106, 0x3727c5ac
	v_pk_fma_f32 v[108:109], v[102:103], s[0:1], v[106:107] op_sel_hi:[1,0,0]
	s_mov_b32 s1, 0x800000
	v_mul_f32_e32 v98, 0x4b800000, v109
	v_cmp_gt_f32_e32 vcc, s1, v109
	v_sub_f32_e32 v107, v101, v135
	ds_read_b128 v[82:85], v150 offset:17984
	v_cndmask_b32_e32 v98, v109, v98, vcc
	v_rsq_f32_e32 v98, v98
	v_sub_f32_e32 v109, v100, v135
	ds_read_b128 v[86:89], v150 offset:18496
	v_sub_f32_e32 v117, v113, v135
	v_mul_f32_e32 v99, 0x45800000, v98
	v_cndmask_b32_e32 v110, v98, v99, vcc
	v_mul_f32_e32 v112, v110, v112
	v_fma_f32 v34, v34, v112, v38
	v_mul_f32_e32 v38, v110, v111
	v_fma_f32 v35, v35, v38, v39
	v_max_f32_e32 v38, 0, v35
	v_mul_f32_e32 v35, v110, v109
	v_mul_f32_e32 v116, v110, v116
	v_fma_f32 v35, v36, v35, v40
	v_mul_f32_e32 v36, v110, v107
	v_fma_f32 v42, v42, v116, v46
	v_mul_f32_e32 v46, v110, v115
	v_fmac_f32_e32 v41, v37, v36
	v_mul_f32_e32 v37, 0x4b800000, v108
	v_cmp_gt_f32_e32 vcc, s1, v108
	v_sub_f32_e32 v113, v105, v135
	v_fma_f32 v43, v43, v46, v47
	v_mul_f32_e32 v46, v110, v114
	v_cndmask_b32_e32 v37, v108, v37, vcc
	v_mul_f32_e32 v135, v110, v163
	v_fma_f32 v44, v44, v46, v48
	v_mul_f32_e32 v46, v110, v113
	v_rsq_f32_e32 v37, v37
	v_fma_f32 v90, v90, v135, v94
	v_mul_f32_e32 v94, v110, v162
	v_fmac_f32_e32 v49, v45, v46
	ds_read_b128 v[98:101], v150 offset:17920
	ds_read_b128 v[102:105], v150 offset:18432
	v_fma_f32 v91, v91, v94, v95
	v_mul_f32_e32 v94, v110, v161
	v_max_f32_e32 v42, 0, v42
	v_max_f32_e32 v43, 0, v43
	v_max_f32_e32 v44, 0, v44
	v_max_f32_e32 v45, 0, v49
	v_max_f32_e32 v34, 0, v34
	v_max_f32_e32 v35, 0, v35
	v_max_f32_e32 v36, 0, v41
	v_fma_f32 v92, v92, v94, v96
	v_mul_f32_e32 v94, v110, v160
	v_mul_f32_e32 v135, v110, v159
	v_cvt_pk_f16_f32 v115, v44, v45
	v_cvt_pk_f16_f32 v114, v42, v43
	v_cvt_pk_f16_f32 v35, v35, v36
	v_cvt_pk_f16_f32 v34, v34, v38
	v_fmac_f32_e32 v97, v93, v94
	s_waitcnt lgkmcnt(2)
	v_fma_f32 v82, v82, v135, v86
	v_mul_f32_e32 v86, v110, v158
	ds_write2_b64 v152, v[114:115], v[34:35] offset0:24 offset1:28
	v_mul_f32_e32 v34, 0x45800000, v37
	ds_read_b128 v[66:69], v150 offset:18048
	ds_read_b128 v[70:73], v150 offset:18560
	v_max_f32_e32 v90, 0, v90
	v_max_f32_e32 v91, 0, v91
	v_max_f32_e32 v92, 0, v92
	v_max_f32_e32 v93, 0, v97
	v_fma_f32 v83, v83, v86, v87
	v_cndmask_b32_e32 v34, v37, v34, vcc
	v_sub_f32_e32 v31, v31, v134
	v_cvt_pk_f16_f32 v137, v92, v93
	v_cvt_pk_f16_f32 v136, v90, v91
	ds_read_b128 v[90:93], v150 offset:17984
	ds_read_b128 v[94:97], v150 offset:18496
	v_max_f32_e32 v86, 0, v83
	v_mul_f32_e32 v83, v110, v156
	v_mul_f32_e32 v31, v34, v31
	v_fma_f32 v83, v84, v83, v88
	v_mul_f32_e32 v84, v110, v154
	s_waitcnt lgkmcnt(5)
	v_fma_f32 v31, v99, v31, v103
	ds_read_b128 v[50:53], v150 offset:18112
	ds_read_b128 v[54:57], v150 offset:18624
	v_fmac_f32_e32 v89, v85, v84
	v_max_f32_e32 v35, 0, v31
	v_sub_f32_e32 v31, v32, v134
	v_sub_f32_e32 v32, v33, v134
	v_max_f32_e32 v82, 0, v82
	v_max_f32_e32 v83, 0, v83
	v_max_f32_e32 v84, 0, v89
	v_mul_f32_e32 v135, v110, v153
	v_mul_f32_e32 v31, v34, v31
	v_mul_f32_e32 v32, v34, v32
	v_sub_f32_e32 v27, v27, v134
	v_cvt_pk_f16_f32 v83, v83, v84
	v_cvt_pk_f16_f32 v82, v82, v86
	s_waitcnt lgkmcnt(4)
	v_fma_f32 v66, v66, v135, v70
	v_mul_f32_e32 v70, v110, v157
	v_fma_f32 v31, v100, v31, v104
	v_fmac_f32_e32 v105, v101, v32
	v_mul_f32_e32 v27, v34, v27
	ds_write2_b64 v152, v[136:137], v[82:83] offset1:4
	ds_read_b128 v[82:85], v150 offset:18048
	ds_read_b128 v[86:89], v150 offset:18560
	v_fma_f32 v67, v67, v70, v71
	v_mul_f32_e32 v70, v110, v155
	v_max_f32_e32 v31, 0, v31
	v_max_f32_e32 v32, 0, v105
	s_waitcnt lgkmcnt(5)
	v_fma_f32 v27, v91, v27, v95
	v_fma_f32 v68, v68, v70, v72
	v_mul_f32_e32 v70, v110, v129
	v_mul_f32_e32 v128, v110, v128
	v_sub_f32_e32 v30, v30, v134
	v_cvt_pk_f16_f32 v31, v31, v32
	v_sub_f32_e32 v26, v26, v134
	v_max_f32_e32 v32, 0, v27
	v_sub_f32_e32 v27, v28, v134
	v_sub_f32_e32 v28, v29, v134
	v_fmac_f32_e32 v73, v69, v70
	s_waitcnt lgkmcnt(3)
	v_fma_f32 v50, v50, v128, v54
	v_mul_f32_e32 v54, v110, v127
	v_mul_f32_e32 v30, v34, v30
	v_mul_f32_e32 v26, v34, v26
	v_mul_f32_e32 v27, v34, v27
	v_mul_f32_e32 v28, v34, v28
	ds_read_b128 v[74:77], v150 offset:18176
	ds_read_b128 v[78:81], v150 offset:18688
	v_max_f32_e32 v66, 0, v66
	v_max_f32_e32 v67, 0, v67
	v_max_f32_e32 v68, 0, v68
	v_max_f32_e32 v69, 0, v73
	v_fma_f32 v51, v51, v54, v55
	v_fma_f32 v30, v98, v30, v102
	v_fma_f32 v26, v90, v26, v94
	v_fma_f32 v27, v92, v27, v96
	v_fmac_f32_e32 v97, v93, v28
	v_sub_f32_e32 v23, v23, v134
	v_cvt_pk_f16_f32 v137, v68, v69
	v_cvt_pk_f16_f32 v136, v66, v67
	ds_read_b128 v[66:69], v150 offset:18112
	ds_read_b128 v[70:73], v150 offset:18624
	v_max_f32_e32 v54, 0, v51
	v_mul_f32_e32 v51, v110, v126
	v_max_f32_e32 v30, 0, v30
	v_max_f32_e32 v26, 0, v26
	v_max_f32_e32 v27, 0, v27
	v_max_f32_e32 v28, 0, v97
	v_mul_f32_e32 v23, v34, v23
	v_fma_f32 v51, v52, v51, v56
	v_mul_f32_e32 v52, v110, v125
	v_cvt_pk_f16_f32 v30, v30, v35
	v_cvt_pk_f16_f32 v27, v27, v28
	v_cvt_pk_f16_f32 v26, v26, v32
	v_add_u32_e32 v28, 0x1000, v152
	s_waitcnt lgkmcnt(4)
	v_fma_f32 v23, v83, v23, v87
	ds_read_b128 v[58:61], v150 offset:18240
	ds_read_b128 v[62:65], v150 offset:18752
	v_fmac_f32_e32 v57, v53, v52
	ds_write2_b64 v28, v[30:31], v[26:27] offset0:32 offset1:36
	v_max_f32_e32 v26, 0, v23
	v_sub_f32_e32 v23, v24, v134
	v_sub_f32_e32 v24, v25, v134
	v_max_f32_e32 v50, 0, v50
	v_max_f32_e32 v51, 0, v51
	v_max_f32_e32 v52, 0, v57
	v_mul_f32_e32 v124, v110, v124
	v_mul_f32_e32 v23, v34, v23
	v_mul_f32_e32 v24, v34, v24
	v_sub_f32_e32 v19, v19, v134
	v_cvt_pk_f16_f32 v51, v51, v52
	v_cvt_pk_f16_f32 v50, v50, v54
	s_waitcnt lgkmcnt(5)
	v_fma_f32 v74, v74, v124, v78
	v_mul_f32_e32 v78, v110, v123
	v_fma_f32 v23, v84, v23, v88
	v_fmac_f32_e32 v89, v85, v24
	v_mul_f32_e32 v19, v34, v19
	ds_write2_b64 v152, v[136:137], v[50:51] offset0:8 offset1:12
	ds_read_b128 v[50:53], v150 offset:18176
	ds_read_b128 v[54:57], v150 offset:18688
	v_fma_f32 v75, v75, v78, v79
	v_mul_f32_e32 v78, v110, v122
	v_max_f32_e32 v23, 0, v23
	v_max_f32_e32 v24, 0, v89
	s_waitcnt lgkmcnt(6)
	v_fma_f32 v19, v67, v19, v71
	v_fma_f32 v76, v76, v78, v80
	v_mul_f32_e32 v78, v110, v121
	v_mul_f32_e32 v119, v110, v119
	v_sub_f32_e32 v22, v22, v134
	v_cvt_pk_f16_f32 v23, v23, v24
	v_sub_f32_e32 v18, v18, v134
	v_max_f32_e32 v24, 0, v19
	v_sub_f32_e32 v19, v20, v134
	v_sub_f32_e32 v20, v21, v134
	v_fmac_f32_e32 v81, v77, v78
	s_waitcnt lgkmcnt(4)
	v_fma_f32 v58, v58, v119, v62
	v_mul_f32_e32 v62, v110, v120
	v_mul_f32_e32 v22, v34, v22
	v_mul_f32_e32 v18, v34, v18
	v_mul_f32_e32 v19, v34, v19
	v_mul_f32_e32 v20, v34, v20
	v_max_f32_e32 v74, 0, v74
	v_max_f32_e32 v75, 0, v75
	v_max_f32_e32 v76, 0, v76
	v_max_f32_e32 v77, 0, v81
	v_fma_f32 v59, v59, v62, v63
	v_fma_f32 v22, v82, v22, v86
	v_fma_f32 v18, v66, v18, v70
	v_fma_f32 v19, v68, v19, v72
	v_fmac_f32_e32 v73, v69, v20
	v_sub_f32_e32 v15, v15, v134
	v_cvt_pk_f16_f32 v123, v76, v77
	v_cvt_pk_f16_f32 v122, v74, v75
	ds_read_b128 v[74:77], v150 offset:18240
	ds_read_b128 v[78:81], v150 offset:18752
	v_max_f32_e32 v62, 0, v59
	v_mul_f32_e32 v59, v110, v118
	v_max_f32_e32 v22, 0, v22
	v_max_f32_e32 v18, 0, v18
	v_max_f32_e32 v19, 0, v19
	v_max_f32_e32 v20, 0, v73
	v_mul_f32_e32 v15, v34, v15
	v_fma_f32 v59, v60, v59, v64
	v_mul_f32_e32 v60, v110, v117
	v_cvt_pk_f16_f32 v22, v22, v26
	v_cvt_pk_f16_f32 v19, v19, v20
	v_cvt_pk_f16_f32 v18, v18, v24
	s_waitcnt lgkmcnt(2)
	v_fma_f32 v15, v51, v15, v55
	v_fmac_f32_e32 v65, v61, v60
	ds_write2_b64 v28, v[22:23], v[18:19] offset0:40 offset1:44
	v_max_f32_e32 v18, 0, v15
	v_sub_f32_e32 v15, v16, v134
	v_sub_f32_e32 v16, v17, v134
	v_max_f32_e32 v58, 0, v58
	v_max_f32_e32 v59, 0, v59
	v_max_f32_e32 v60, 0, v65
	v_mul_f32_e32 v15, v34, v15
	v_mul_f32_e32 v16, v34, v16
	v_sub_f32_e32 v11, v11, v134
	v_cvt_pk_f16_f32 v59, v59, v60
	v_cvt_pk_f16_f32 v58, v58, v62
	v_fma_f32 v15, v52, v15, v56
	v_fmac_f32_e32 v57, v53, v16
	v_mul_f32_e32 v11, v34, v11
	ds_write2_b64 v152, v[122:123], v[58:59] offset0:16 offset1:20
	ds_read_b128 v[58:61], v150 offset:18304
	ds_read_b128 v[62:65], v150 offset:18816
	v_max_f32_e32 v15, 0, v15
	v_max_f32_e32 v16, 0, v57
	s_waitcnt lgkmcnt(4)
	v_fma_f32 v11, v75, v11, v79
	v_sub_f32_e32 v14, v14, v134
	v_cvt_pk_f16_f32 v15, v15, v16
	v_sub_f32_e32 v10, v10, v134
	v_max_f32_e32 v16, 0, v11
	v_sub_f32_e32 v11, v12, v134
	v_sub_f32_e32 v12, v13, v134
	v_mul_f32_e32 v14, v34, v14
	v_mul_f32_e32 v10, v34, v10
	v_mul_f32_e32 v11, v34, v11
	v_mul_f32_e32 v12, v34, v12
	v_fma_f32 v14, v50, v14, v54
	v_fma_f32 v10, v74, v10, v78
	v_fma_f32 v11, v76, v11, v80
	v_fmac_f32_e32 v81, v77, v12
	v_sub_f32_e32 v7, v7, v134
	ds_read_b128 v[42:45], v150 offset:18368
	ds_read_b128 v[46:49], v150 offset:18880
	v_max_f32_e32 v14, 0, v14
	v_max_f32_e32 v10, 0, v10
	v_max_f32_e32 v11, 0, v11
	v_max_f32_e32 v12, 0, v81
	v_mul_f32_e32 v7, v34, v7
	v_cvt_pk_f16_f32 v14, v14, v18
	v_cvt_pk_f16_f32 v11, v11, v12
	v_cvt_pk_f16_f32 v10, v10, v16
	s_waitcnt lgkmcnt(2)
	v_fma_f32 v7, v59, v7, v63
	ds_write2_b64 v28, v[14:15], v[10:11] offset0:48 offset1:52
	v_max_f32_e32 v10, 0, v7
	v_sub_f32_e32 v7, v8, v134
	v_sub_f32_e32 v8, v9, v134
	v_mul_f32_e32 v7, v34, v7
	v_mul_f32_e32 v8, v34, v8
	v_sub_f32_e32 v3, v3, v134
	v_fma_f32 v7, v60, v7, v64
	v_fmac_f32_e32 v65, v61, v8
	v_mul_f32_e32 v3, v34, v3
	v_max_f32_e32 v7, 0, v7
	v_max_f32_e32 v8, 0, v65
	s_waitcnt lgkmcnt(1)
	v_fma_f32 v3, v43, v3, v47
	v_sub_f32_e32 v6, v6, v134
	v_cvt_pk_f16_f32 v7, v7, v8
	v_sub_f32_e32 v2, v2, v134
	v_max_f32_e32 v8, 0, v3
	v_sub_f32_e32 v3, v4, v134
	v_sub_f32_e32 v4, v5, v134
	v_mul_f32_e32 v6, v34, v6
	v_mul_f32_e32 v2, v34, v2
	v_mul_f32_e32 v3, v34, v3
	v_mul_f32_e32 v4, v34, v4
	v_fma_f32 v6, v58, v6, v62
	v_fma_f32 v2, v42, v2, v46
	v_fma_f32 v3, v44, v3, v48
	v_fmac_f32_e32 v49, v45, v4
	v_max_f32_e32 v6, 0, v6
	v_max_f32_e32 v2, 0, v2
	v_max_f32_e32 v3, 0, v3
	v_max_f32_e32 v4, 0, v49
	v_cvt_pk_f16_f32 v6, v6, v10
	v_cvt_pk_f16_f32 v3, v3, v4
	v_cvt_pk_f16_f32 v2, v2, v8
	ds_write2_b64 v28, v[6:7], v[2:3] offset0:56 offset1:60
	v_lshl_add_u64 v[34:35], s[36:37], 0, v[132:133]
	v_add_co_u32_e32 v74, vcc, s9, v34
	global_load_dwordx4 v[66:69], v132, s[36:37]
	s_nop 0
	v_addc_co_u32_e32 v75, vcc, 0, v35, vcc
	v_add_co_u32_e32 v76, vcc, s11, v34
	ds_read_b128 v[116:119], v151
	s_nop 0
	v_addc_co_u32_e32 v77, vcc, 0, v35, vcc
	global_load_dwordx4 v[88:91], v[76:77], off offset:-4096
	v_add_co_u32_e32 v78, vcc, s12, v34
	global_load_dwordx4 v[70:73], v[76:77], off
	s_nop 0
	v_addc_co_u32_e32 v79, vcc, 0, v35, vcc
	v_add_co_u32_e32 v80, vcc, s8, v34
	ds_read_b128 v[120:123], v151 offset:4352
	s_nop 0
	v_addc_co_u32_e32 v81, vcc, 0, v35, vcc
	global_load_dwordx4 v[92:95], v[80:81], off offset:-4096
	v_add_co_u32_e32 v82, vcc, s10, v34
	global_load_dwordx4 v[96:99], v[80:81], off
	s_nop 0
	v_addc_co_u32_e32 v83, vcc, 0, v35, vcc
	v_add_co_u32_e32 v84, vcc, s7, v34
	ds_read_b128 v[164:167], v151 offset:4416
	s_nop 0
	v_addc_co_u32_e32 v85, vcc, 0, v35, vcc
	global_load_dwordx4 v[108:111], v[84:85], off
	global_load_dwordx4 v[100:103], v[84:85], off offset:-4096
	v_add_co_u32_e32 v86, vcc, s6, v34
	s_nop 1
	v_addc_co_u32_e32 v87, vcc, 0, v35, vcc
	global_load_dwordx4 v[112:115], v[86:87], off
	global_load_dwordx4 v[58:61], v132, s[36:37] offset:1024
	global_load_dwordx4 v[62:65], v[74:75], off offset:1024
	global_load_dwordx4 v[34:37], v[76:77], off offset:1024
	global_load_dwordx4 v[54:57], v[78:79], off offset:1024
	global_load_dwordx4 v[50:53], v[80:81], off offset:1024
	global_load_dwordx4 v[46:49], v[82:83], off offset:1024
	global_load_dwordx4 v[42:45], v[84:85], off offset:1024
	global_load_dwordx4 v[38:41], v[86:87], off offset:1024
	ds_read_b128 v[30:33], v147 offset:18944
	ds_read_b128 v[26:29], v147 offset:19008
	s_waitcnt vmcnt(15) lgkmcnt(1)
	v_mfma_f32_16x16x32_f16 v[124:127], v[66:69], v[116:119], v[30:33]
	v_mfma_f32_16x16x32_f16 v[66:69], v[66:69], v[120:123], v[30:33]
	s_waitcnt vmcnt(14) lgkmcnt(0)
	v_mfma_f32_16x16x32_f16 v[134:137], v[88:91], v[116:119], v[26:29]
	v_mfma_f32_16x16x32_f16 v[88:91], v[88:91], v[120:123], v[26:29]
	global_load_dwordx4 v[30:33], v132, s[36:37] offset:2048
	s_nop 1
	global_load_dwordx4 v[26:29], v[74:75], off offset:2048
	ds_read_b128 v[22:25], v147 offset:19072
	ds_read_b128 v[18:21], v147 offset:19136
	s_waitcnt vmcnt(15) lgkmcnt(1)
	v_mfma_f32_16x16x32_f16 v[138:141], v[70:73], v[116:119], v[22:25]
	v_mfma_f32_16x16x32_f16 v[70:73], v[70:73], v[120:123], v[22:25]
	s_waitcnt vmcnt(14) lgkmcnt(0)
	v_mfma_f32_16x16x32_f16 v[142:145], v[92:95], v[116:119], v[18:21]
	v_mfma_f32_16x16x32_f16 v[92:95], v[92:95], v[120:123], v[18:21]
	global_load_dwordx4 v[22:25], v[76:77], off offset:2048
	s_nop 1
	global_load_dwordx4 v[18:21], v[78:79], off offset:2048
	ds_read_b128 v[6:9], v147 offset:19328
	s_waitcnt vmcnt(14) lgkmcnt(0)
	v_mfma_f32_16x16x32_f16 v[160:163], v[108:111], v[116:119], v[6:9]
	v_mfma_f32_16x16x32_f16 v[108:111], v[108:111], v[120:123], v[6:9]
	s_nop 2
	global_load_dwordx4 v[6:9], v[84:85], off offset:2048
	ds_read_b128 v[10:13], v147 offset:19264
	s_waitcnt vmcnt(14) lgkmcnt(0)
	v_mfma_f32_16x16x32_f16 v[156:159], v[100:103], v[116:119], v[10:13]
	v_mfma_f32_16x16x32_f16 v[100:103], v[100:103], v[120:123], v[10:13]
	s_nop 2
	global_load_dwordx4 v[10:13], v[82:83], off offset:2048
	ds_read_b128 v[14:17], v147 offset:19200
	s_waitcnt lgkmcnt(0)
	v_mfma_f32_16x16x32_f16 v[152:155], v[96:99], v[116:119], v[14:17]
	ds_read_b128 v[2:5], v147 offset:19392
	s_waitcnt vmcnt(14) lgkmcnt(0)
	v_mfma_f32_16x16x32_f16 v[116:119], v[112:115], v[116:119], v[2:5]
	v_mfma_f32_16x16x32_f16 v[112:115], v[112:115], v[120:123], v[2:5]
	s_nop 2
	global_load_dwordx4 v[2:5], v[86:87], off offset:2048
	v_mfma_f32_16x16x32_f16 v[96:99], v[96:99], v[120:123], v[14:17]
	ds_read_b128 v[120:123], v151 offset:64
	s_nop 1
	global_load_dwordx4 v[14:17], v[80:81], off offset:2048
	s_waitcnt vmcnt(15) lgkmcnt(0)
	v_mfma_f32_16x16x32_f16 v[124:127], v[58:61], v[120:123], v[124:127]
	v_mfma_f32_16x16x32_f16 v[58:61], v[58:61], v[164:167], v[66:69]
	s_waitcnt vmcnt(14)
	v_mfma_f32_16x16x32_f16 v[66:69], v[62:65], v[120:123], v[134:137]
	v_mfma_f32_16x16x32_f16 v[62:65], v[62:65], v[164:167], v[88:91]
	s_nop 1
	global_load_dwordx4 v[134:137], v[82:83], off offset:3072
	s_nop 0
	global_load_dwordx4 v[82:85], v[84:85], off offset:3072
	s_waitcnt vmcnt(15)
	v_mfma_f32_16x16x32_f16 v[88:91], v[34:37], v[120:123], v[138:141]
	v_mfma_f32_16x16x32_f16 v[34:37], v[34:37], v[164:167], v[70:73]
	s_nop 1
	global_load_dwordx4 v[138:141], v[86:87], off offset:3072
	s_waitcnt vmcnt(15)
	v_mfma_f32_16x16x32_f16 v[70:73], v[54:57], v[120:123], v[142:145]
	v_mfma_f32_16x16x32_f16 v[54:57], v[54:57], v[164:167], v[92:95]
	s_nop 1
	ds_read_b128 v[142:145], v151 offset:128
	s_waitcnt vmcnt(14)
	v_mfma_f32_16x16x32_f16 v[92:95], v[50:53], v[120:123], v[152:155]
	v_mfma_f32_16x16x32_f16 v[50:53], v[50:53], v[164:167], v[96:99]
	s_nop 1
	ds_read_b128 v[152:155], v151 offset:4480
	s_waitcnt vmcnt(13)
	v_mfma_f32_16x16x32_f16 v[96:99], v[46:49], v[120:123], v[156:159]
	v_mfma_f32_16x16x32_f16 v[46:49], v[46:49], v[164:167], v[100:103]
	s_waitcnt vmcnt(12)
	v_mfma_f32_16x16x32_f16 v[100:103], v[42:45], v[120:123], v[160:163]
	v_mfma_f32_16x16x32_f16 v[42:45], v[42:45], v[164:167], v[108:111]
	s_waitcnt vmcnt(11)
	v_mfma_f32_16x16x32_f16 v[108:111], v[38:41], v[120:123], v[116:119]
	global_load_dwordx4 v[120:123], v[78:79], off offset:3072
	s_nop 0
	global_load_dwordx4 v[78:81], v[80:81], off offset:3072
	s_nop 0
	global_load_dwordx4 v[116:119], v[74:75], off offset:3072
	v_mfma_f32_16x16x32_f16 v[38:41], v[38:41], v[164:167], v[112:115]
	global_load_dwordx4 v[74:77], v[76:77], off offset:3072
	s_nop 1
	global_load_dwordx4 v[112:115], v132, s[36:37] offset:3072
	s_waitcnt vmcnt(15) lgkmcnt(1)
	v_mfma_f32_16x16x32_f16 v[124:127], v[30:33], v[142:145], v[124:127]
	s_waitcnt lgkmcnt(0)
	v_mfma_f32_16x16x32_f16 v[30:33], v[30:33], v[152:155], v[58:61]
	s_waitcnt vmcnt(14)
	v_mfma_f32_16x16x32_f16 v[58:61], v[26:29], v[142:145], v[66:69]
	v_mfma_f32_16x16x32_f16 v[26:29], v[26:29], v[152:155], v[62:65]
	s_waitcnt vmcnt(13)
	v_mfma_f32_16x16x32_f16 v[62:65], v[22:25], v[142:145], v[88:91]
	v_mfma_f32_16x16x32_f16 v[22:25], v[22:25], v[152:155], v[34:37]
	s_waitcnt vmcnt(12)
	v_mfma_f32_16x16x32_f16 v[34:37], v[18:21], v[142:145], v[70:73]
	s_waitcnt vmcnt(8)
	v_mfma_f32_16x16x32_f16 v[66:69], v[14:17], v[142:145], v[92:95]
	v_mfma_f32_16x16x32_f16 v[86:89], v[10:13], v[142:145], v[96:99]
	v_mfma_f32_16x16x32_f16 v[94:97], v[6:9], v[142:145], v[100:103]
	v_mfma_f32_16x16x32_f16 v[102:105], v[2:5], v[142:145], v[108:111]
	ds_read_b128 v[142:145], v151 offset:4544
	s_nop 1
	ds_read_b128 v[108:111], v151 offset:192
	v_mfma_f32_16x16x32_f16 v[18:21], v[18:21], v[152:155], v[54:57]
	v_mfma_f32_16x16x32_f16 v[70:73], v[14:17], v[152:155], v[50:53]
	v_mfma_f32_16x16x32_f16 v[90:93], v[10:13], v[152:155], v[46:49]
	v_mfma_f32_16x16x32_f16 v[98:101], v[6:9], v[152:155], v[42:45]
	v_mfma_f32_16x16x32_f16 v[2:5], v[2:5], v[152:155], v[38:41]
	s_waitcnt vmcnt(0) lgkmcnt(1)
	v_mfma_f32_16x16x32_f16 v[6:9], v[112:115], v[142:145], v[30:33]
	s_waitcnt lgkmcnt(0)
	v_mfma_f32_16x16x32_f16 v[50:53], v[116:119], v[108:111], v[58:61]
	v_mfma_f32_16x16x32_f16 v[10:13], v[116:119], v[142:145], v[26:29]
	v_mfma_f32_16x16x32_f16 v[54:57], v[74:77], v[108:111], v[62:65]
	v_mfma_f32_16x16x32_f16 v[14:17], v[74:77], v[142:145], v[22:25]
	v_mfma_f32_16x16x32_f16 v[18:21], v[120:123], v[142:145], v[18:21]
	v_mfma_f32_16x16x32_f16 v[22:25], v[78:81], v[142:145], v[70:73]
	v_mfma_f32_16x16x32_f16 v[26:29], v[134:137], v[142:145], v[90:93]
	v_mfma_f32_16x16x32_f16 v[30:33], v[82:85], v[142:145], v[98:101]
	v_mfma_f32_16x16x32_f16 v[2:5], v[138:141], v[142:145], v[2:5]
	v_mfma_f32_16x16x32_f16 v[46:49], v[112:115], v[108:111], v[124:127]
	v_mfma_f32_16x16x32_f16 v[58:61], v[120:123], v[108:111], v[34:37]
	v_mfma_f32_16x16x32_f16 v[62:65], v[78:81], v[108:111], v[66:69]
	v_mfma_f32_16x16x32_f16 v[42:45], v[134:137], v[108:111], v[86:89]
	v_mfma_f32_16x16x32_f16 v[38:41], v[82:85], v[108:111], v[94:97]
	v_mfma_f32_16x16x32_f16 v[34:37], v[138:141], v[108:111], v[102:105]
	s_nop 2
	v_lshrrev_b32_e32 v104, 5, v146
	v_lshlrev_b32_e32 v66, 2, v104
	v_lshl_or_b32 v105, v1, 7, v66
	ds_read_b32 v70, v105 offset:20480
	ds_read_b128 v[112:115], v150 offset:19776
	v_add_u32_e32 v82, 0x5000, v105
	ds_read2_b32 v[68:69], v82 offset1:2
	ds_read2_b32 v[78:79], v82 offset0:4 offset1:6
	v_lshlrev_b32_e32 v0, 4, v0
	v_and_b32_e32 v132, 0x1f0, v0
	v_lshl_add_u64 v[66:67], s[4:5], 0, v[132:133]
	v_add_u32_e32 v83, v130, v132
	v_lshl_add_u64 v[0:1], s[2:3], 0, v[132:133]
	ds_read2_b32 v[80:81], v82 offset0:8 offset1:10
	s_waitcnt lgkmcnt(4)
	v_max_i32_e32 v132, 0, v70
	v_lshlrev_b64 v[70:71], 9, v[132:133]
	s_waitcnt lgkmcnt(2)
	v_max_i32_e32 v132, 0, v69
	v_lshlrev_b64 v[72:73], 9, v[132:133]
	s_waitcnt lgkmcnt(1)
	v_max_i32_e32 v132, 0, v78
	v_lshlrev_b64 v[84:85], 9, v[132:133]
	v_max_i32_e32 v132, 0, v79
	v_lshlrev_b64 v[78:79], 9, v[132:133]
	v_lshl_add_u64 v[84:85], v[66:67], 0, v[84:85]
	v_lshl_add_u64 v[78:79], v[66:67], 0, v[78:79]
	s_waitcnt lgkmcnt(0)
	v_max_i32_e32 v132, 0, v80
	global_load_dwordx4 v[84:87], v[84:85], off nt
	v_lshl_add_u64 v[70:71], v[66:67], 0, v[70:71]
	global_load_dwordx4 v[88:91], v[78:79], off nt
	v_lshlrev_b64 v[78:79], 9, v[132:133]
	v_max_i32_e32 v132, 0, v81
	ds_read2_b32 v[80:81], v82 offset0:12 offset1:14
	v_lshlrev_b64 v[92:93], 9, v[132:133]
	v_lshl_add_u64 v[78:79], v[66:67], 0, v[78:79]
	v_lshl_add_u64 v[96:97], v[66:67], 0, v[92:93]
	global_load_dwordx4 v[92:95], v[78:79], off nt
	s_waitcnt lgkmcnt(0)
	v_max_i32_e32 v132, 0, v80
	global_load_dwordx4 v[96:99], v[96:97], off nt
	v_lshlrev_b64 v[78:79], 9, v[132:133]
	v_max_i32_e32 v132, 0, v81
	v_lshlrev_b64 v[80:81], 9, v[132:133]
	v_lshl_add_u64 v[74:75], v[66:67], 0, v[72:73]
	v_lshl_add_u64 v[78:79], v[66:67], 0, v[78:79]
	v_lshl_add_u64 v[80:81], v[66:67], 0, v[80:81]
	global_load_dwordx4 v[70:73], v[70:71], off nt
	s_movk_i32 s2, 0x220
	global_load_dwordx4 v[74:77], v[74:75], off nt
	v_mov_b32_e32 v69, 0x440
	global_load_dwordx4 v[100:103], v[78:79], off nt
	global_load_dwordx4 v[108:111], v[80:81], off nt
	v_mov_b32_e32 v78, 0x880
	v_mad_u32_u24 v69, v104, s2, v69
	v_mad_u32_u24 v78, v104, s2, v78
	v_mad_u32_u24 v107, v131, s2, v130
	v_mad_u32_u24 v79, v104, s2, v83
	v_add_u32_e32 v81, v83, v69
	v_add_u32_e32 v80, v83, v78
	v_add_u32_e32 v82, v107, v147
	s_load_dword s0, s[34:35], 0x0
	v_mul_u32_u24_e32 v69, 0x220, v104
	ds_read_b128 v[120:123], v150 offset:20288
	ds_read_b128 v[128:131], v150 offset:20352
	ds_read_b128 v[134:137], v150 offset:20416
	ds_read_b128 v[116:119], v150 offset:20224
	ds_read_b128 v[124:127], v150 offset:19904
	s_waitcnt vmcnt(7)
	ds_write_b128 v80, v[84:87]
	s_waitcnt vmcnt(6)
	ds_write_b128 v80, v[88:91] offset:1088
	s_waitcnt vmcnt(5)
	ds_write_b128 v80, v[92:95] offset:2176
	s_waitcnt vmcnt(4)
	ds_write_b128 v80, v[96:99] offset:3264
	s_waitcnt vmcnt(3)
	ds_write_b128 v79, v[70:73]
	s_waitcnt vmcnt(2)
	ds_write_b128 v81, v[74:77]
	s_waitcnt vmcnt(1)
	ds_write_b128 v80, v[100:103] offset:4352
	s_waitcnt vmcnt(0)
	ds_write_b128 v80, v[108:111] offset:5440
	ds_read_b128 v[70:73], v82
	ds_read_b128 v[84:87], v82 offset:64
	ds_read_b128 v[88:91], v82 offset:128
	ds_read_b128 v[92:95], v82 offset:192
	ds_read_b128 v[96:99], v82 offset:256
	ds_read_b128 v[100:103], v82 offset:320
	s_waitcnt lgkmcnt(0)
	v_pk_fma_f32 v[78:79], s[0:1], v[46:47], v[70:71] op_sel_hi:[0,1,1]
	v_pk_fma_f32 v[76:77], s[0:1], v[48:49], v[72:73] op_sel_hi:[0,1,1]
	v_pk_fma_f32 v[74:75], s[0:1], v[50:51], v[84:85] op_sel_hi:[0,1,1]
	v_pk_fma_f32 v[72:73], s[0:1], v[52:53], v[86:87] op_sel_hi:[0,1,1]
	v_pk_fma_f32 v[70:71], s[0:1], v[54:55], v[88:89] op_sel_hi:[0,1,1]
	v_pk_fma_f32 v[54:55], s[0:1], v[56:57], v[90:91] op_sel_hi:[0,1,1]
	v_pk_fma_f32 v[52:53], s[0:1], v[58:59], v[92:93] op_sel_hi:[0,1,1]
	v_pk_fma_f32 v[50:51], s[0:1], v[60:61], v[94:95] op_sel_hi:[0,1,1]
	v_pk_fma_f32 v[48:49], s[0:1], v[62:63], v[96:97] op_sel_hi:[0,1,1]
	v_mov_b32_e32 v56, v78
	v_mov_b32_e32 v57, v74
	v_mov_b32_e32 v58, v79
	v_mov_b32_e32 v59, v75
	v_mov_b32_e32 v60, v76
	v_mov_b32_e32 v61, v72
	v_mov_b32_e32 v62, v77
	v_mov_b32_e32 v63, v73
	v_pk_fma_f32 v[46:47], s[0:1], v[64:65], v[98:99] op_sel_hi:[0,1,1]
	v_mov_b32_e32 v64, v70
	v_mov_b32_e32 v65, v54
	v_mov_b32_e32 v84, v71
	v_mov_b32_e32 v85, v55
	v_pk_add_f32 v[56:57], v[56:57], v[58:59]
	v_pk_add_f32 v[58:59], v[60:61], v[62:63]
	v_pk_add_f32 v[60:61], v[64:65], v[84:85]
	v_pk_add_f32 v[56:57], v[56:57], v[58:59]
	v_pk_add_f32 v[86:87], v[52:53], v[52:53] op_sel:[0,1] op_sel_hi:[1,0]
	v_pk_add_f32 v[88:89], v[50:51], v[50:51] op_sel:[0,1] op_sel_hi:[1,0]
	v_pk_add_f32 v[58:59], v[60:61], v[60:61] op_sel:[0,1] op_sel_hi:[1,0]
	v_add_f32_e32 v56, 0, v56
	v_mov_b32_e32 v91, v48
	v_mov_b32_e32 v87, v46
	v_mov_b32_e32 v89, v47
	v_mov_b32_e32 v59, v49
	v_add_f32_e32 v90, v56, v57
	v_pk_fma_f32 v[42:43], s[0:1], v[42:43], v[100:101] op_sel_hi:[0,1,1]
	v_pk_fma_f32 v[44:45], s[0:1], v[44:45], v[102:103] op_sel_hi:[0,1,1]
	v_pk_add_f32 v[60:61], v[86:87], v[88:89]
	v_pk_add_f32 v[56:57], v[90:91], v[58:59]
	v_mov_b32_e32 v92, v42
	v_pk_add_f32 v[56:57], v[56:57], v[60:61]
	v_mov_b32_e32 v93, v44
	v_mov_b32_e32 v60, v43
	v_mov_b32_e32 v61, v45
	v_pk_add_f32 v[64:65], v[56:57], v[56:57] op_sel:[0,1] op_sel_hi:[1,0]
	ds_read_b128 v[56:59], v82 offset:384
	v_pk_add_f32 v[60:61], v[92:93], v[60:61]
	ds_read_b128 v[96:99], v150 offset:20096
	v_pk_add_f32 v[84:85], v[60:61], v[60:61] op_sel:[0,1] op_sel_hi:[1,0]
	ds_read_b128 v[60:63], v82 offset:448
	s_waitcnt lgkmcnt(2)
	v_pk_fma_f32 v[88:89], s[0:1], v[38:39], v[56:57] op_sel_hi:[0,1,1]
	v_pk_fma_f32 v[40:41], s[0:1], v[40:41], v[58:59] op_sel_hi:[0,1,1]
	v_pk_add_f32 v[38:39], v[88:89], v[88:89] op_sel:[0,1] op_sel_hi:[1,0]
	v_pk_add_f32 v[56:57], v[40:41], v[40:41] op_sel:[0,1] op_sel_hi:[1,0]
	s_waitcnt lgkmcnt(0)
	v_pk_fma_f32 v[90:91], s[0:1], v[34:35], v[60:61] op_sel_hi:[0,1,1]
	v_pk_fma_f32 v[92:93], s[0:1], v[36:37], v[62:63] op_sel_hi:[0,1,1]
	v_mov_b32_e32 v65, v90
	v_mov_b32_e32 v85, v91
	v_mov_b32_e32 v39, v92
	v_mov_b32_e32 v57, v93
	v_pk_add_f32 v[34:35], v[64:65], v[84:85]
	v_pk_add_f32 v[36:37], v[38:39], v[56:57]
	ds_read_b128 v[62:65], v150 offset:19968
	v_pk_add_f32 v[34:35], v[34:35], v[36:37]
	ds_read_b128 v[36:39], v150 offset:19456
	ds_read_b128 v[58:61], v150 offset:19520
	v_add_f32_e32 v34, v34, v35
	ds_bpermute_b32 v35, v149, v34
	ds_read_b128 v[84:87], v150 offset:20032
	v_add_u32_e32 v57, v107, v150
	ds_read_b128 v[100:103], v150 offset:20160
	ds_read_b128 v[108:111], v150 offset:19712
	s_waitcnt lgkmcnt(3)
	v_add_f32_e32 v34, v34, v35
	ds_bpermute_b32 v35, v148, v34
	v_or_b32_e32 v56, 0x5000, v105
	s_waitcnt lgkmcnt(0)
	v_add_f32_e32 v35, v34, v35
	v_fmamk_f32 v95, v35, 0xbc000000, v79
	v_fmamk_f32 v94, v35, 0xbc000000, v78
	v_mul_f32_e32 v95, v95, v95
	v_fmac_f32_e32 v95, v94, v94
	v_fmamk_f32 v94, v35, 0xbc000000, v76
	v_fmac_f32_e32 v95, v94, v94
	v_fmamk_f32 v94, v35, 0xbc000000, v77
	v_fmac_f32_e32 v95, v94, v94
	v_fmamk_f32 v94, v35, 0xbc000000, v74
	v_fmac_f32_e32 v95, v94, v94
	v_fmamk_f32 v94, v35, 0xbc000000, v75
	v_fmac_f32_e32 v95, v94, v94
	v_fmamk_f32 v94, v35, 0xbc000000, v72
	v_fmac_f32_e32 v95, v94, v94
	v_fmamk_f32 v94, v35, 0xbc000000, v73
	v_fmac_f32_e32 v95, v94, v94
	v_fmamk_f32 v94, v35, 0xbc000000, v70
	v_fmac_f32_e32 v95, v94, v94
	v_fmamk_f32 v94, v35, 0xbc000000, v71
	v_fmac_f32_e32 v95, v94, v94
	v_fmamk_f32 v94, v35, 0xbc000000, v54
	v_fmac_f32_e32 v95, v94, v94
	v_fmamk_f32 v94, v35, 0xbc000000, v55
	v_fmac_f32_e32 v95, v94, v94
	v_fmamk_f32 v94, v35, 0xbc000000, v52
	v_fmac_f32_e32 v95, v94, v94
	v_fmamk_f32 v94, v35, 0xbc000000, v53
	v_fmac_f32_e32 v95, v94, v94
	v_fmamk_f32 v94, v35, 0xbc000000, v50
	v_fmac_f32_e32 v95, v94, v94
	v_fmamk_f32 v94, v35, 0xbc000000, v51
	v_fmac_f32_e32 v95, v94, v94
	v_fmamk_f32 v94, v35, 0xbc000000, v48
	v_fmac_f32_e32 v95, v94, v94
	v_fmamk_f32 v94, v35, 0xbc000000, v49
	v_fmac_f32_e32 v95, v94, v94
	v_fmamk_f32 v94, v35, 0xbc000000, v46
	v_fmac_f32_e32 v95, v94, v94
	v_fmamk_f32 v94, v35, 0xbc000000, v47
	v_fmac_f32_e32 v95, v94, v94
	v_fmamk_f32 v94, v35, 0xbc000000, v42
	v_fmac_f32_e32 v95, v94, v94
	v_fmamk_f32 v94, v35, 0xbc000000, v43
	v_mul_f32_e32 v34, 0x3c000000, v35
	v_fmac_f32_e32 v95, v94, v94
	v_fmamk_f32 v94, v35, 0xbc000000, v44
	v_fmamk_f32 v35, v35, 0xbc000000, v45
	v_fmac_f32_e32 v95, v94, v94
	v_pk_add_f32 v[138:139], v[88:89], v[34:35] op_sel_hi:[1,0] neg_lo:[0,1] neg_hi:[0,1]
	v_fmac_f32_e32 v95, v35, v35
	v_pk_mul_f32 v[88:89], v[138:139], v[138:139]
	s_nop 0
	v_add_f32_e32 v35, v88, v95
	v_add_f32_e32 v35, v89, v35
	v_pk_add_f32 v[40:41], v[40:41], v[34:35] op_sel_hi:[1,0] neg_lo:[0,1] neg_hi:[0,1]
	s_nop 0
	v_pk_mul_f32 v[88:89], v[40:41], v[40:41]
	s_nop 0
	v_add_f32_e32 v35, v88, v35
	v_add_f32_e32 v35, v89, v35
	v_pk_add_f32 v[140:141], v[90:91], v[34:35] op_sel_hi:[1,0] neg_lo:[0,1] neg_hi:[0,1]
	s_nop 0
	v_pk_mul_f32 v[88:89], v[140:141], v[140:141]
	s_nop 0
	v_add_f32_e32 v35, v88, v35
	v_add_f32_e32 v35, v89, v35
	v_pk_add_f32 v[142:143], v[92:93], v[34:35] op_sel_hi:[1,0] neg_lo:[0,1] neg_hi:[0,1]
	ds_read_b128 v[92:95], v150 offset:19648
	v_pk_mul_f32 v[88:89], v[142:143], v[142:143]
	s_nop 0
	v_add_f32_e32 v35, v88, v35
	v_add_f32_e32 v35, v89, v35
	ds_bpermute_b32 v104, v149, v35
	ds_read_b128 v[88:91], v150 offset:19584
	s_waitcnt lgkmcnt(1)
	v_add_f32_e32 v35, v35, v104
	ds_bpermute_b32 v104, v148, v35
	s_waitcnt lgkmcnt(0)
	v_add_f32_e32 v35, v35, v104
	v_fmac_f32_e32 v106, 0x3c000000, v35
	v_mul_f32_e32 v35, 0x4b800000, v106
	v_cmp_gt_f32_e32 vcc, s1, v106
	s_nop 1
	v_cndmask_b32_e32 v35, v106, v35, vcc
	v_rsq_f32_e32 v35, v35
	ds_read_b128 v[104:107], v150 offset:19840
	v_mul_f32_e32 v132, 0x45800000, v35
	v_cndmask_b32_e32 v132, v35, v132, vcc
	v_pk_add_f32 v[78:79], v[78:79], v[34:35] op_sel_hi:[1,0] neg_lo:[0,1] neg_hi:[0,1]
	v_cmp_lt_i32_e32 vcc, -1, v68
	v_pk_mul_f32 v[78:79], v[132:133], v[78:79] op_sel_hi:[0,1]
	v_pk_fma_f32 v[36:37], v[36:37], v[78:79], v[62:63]
	v_pk_add_f32 v[62:63], v[76:77], v[34:35] op_sel_hi:[1,0] neg_lo:[0,1] neg_hi:[0,1]
	s_nop 0
	v_pk_mul_f32 v[62:63], v[132:133], v[62:63] op_sel_hi:[0,1]
	v_pk_fma_f32 v[38:39], v[38:39], v[62:63], v[64:65]
	ds_write_b128 v57, v[36:39]
	v_pk_add_f32 v[36:37], v[74:75], v[34:35] op_sel_hi:[1,0] neg_lo:[0,1] neg_hi:[0,1]
	v_pk_add_f32 v[38:39], v[72:73], v[34:35] op_sel_hi:[1,0] neg_lo:[0,1] neg_hi:[0,1]
	v_pk_mul_f32 v[36:37], v[132:133], v[36:37] op_sel_hi:[0,1]
	v_pk_mul_f32 v[38:39], v[132:133], v[38:39] op_sel_hi:[0,1]
	v_pk_fma_f32 v[36:37], v[58:59], v[36:37], v[84:85]
	v_pk_fma_f32 v[38:39], v[60:61], v[38:39], v[86:87]
	ds_write_b128 v57, v[36:39] offset:64
	v_pk_add_f32 v[36:37], v[70:71], v[34:35] op_sel_hi:[1,0] neg_lo:[0,1] neg_hi:[0,1]
	v_pk_add_f32 v[38:39], v[54:55], v[34:35] op_sel_hi:[1,0] neg_lo:[0,1] neg_hi:[0,1]
	v_pk_mul_f32 v[36:37], v[132:133], v[36:37] op_sel_hi:[0,1]
	v_pk_mul_f32 v[38:39], v[132:133], v[38:39] op_sel_hi:[0,1]
	v_pk_fma_f32 v[36:37], v[88:89], v[36:37], v[96:97]
	v_pk_fma_f32 v[38:39], v[90:91], v[38:39], v[98:99]
	ds_write_b128 v57, v[36:39] offset:128
	v_pk_add_f32 v[36:37], v[52:53], v[34:35] op_sel_hi:[1,0] neg_lo:[0,1] neg_hi:[0,1]
	v_pk_add_f32 v[38:39], v[50:51], v[34:35] op_sel_hi:[1,0] neg_lo:[0,1] neg_hi:[0,1]
	v_pk_mul_f32 v[36:37], v[132:133], v[36:37] op_sel_hi:[0,1]
	v_pk_mul_f32 v[38:39], v[132:133], v[38:39] op_sel_hi:[0,1]
	v_pk_fma_f32 v[36:37], v[92:93], v[36:37], v[100:101]
	v_pk_fma_f32 v[38:39], v[94:95], v[38:39], v[102:103]
	ds_write_b128 v57, v[36:39] offset:192
	v_pk_add_f32 v[36:37], v[48:49], v[34:35] op_sel_hi:[1,0] neg_lo:[0,1] neg_hi:[0,1]
	v_pk_add_f32 v[38:39], v[46:47], v[34:35] op_sel_hi:[1,0] neg_lo:[0,1] neg_hi:[0,1]
	v_pk_mul_f32 v[36:37], v[132:133], v[36:37] op_sel_hi:[0,1]
	v_pk_mul_f32 v[38:39], v[132:133], v[38:39] op_sel_hi:[0,1]
	v_pk_fma_f32 v[36:37], v[108:109], v[36:37], v[116:117]
	v_pk_fma_f32 v[38:39], v[110:111], v[38:39], v[118:119]
	ds_write_b128 v57, v[36:39] offset:256
	v_pk_add_f32 v[36:37], v[42:43], v[34:35] op_sel_hi:[1,0] neg_lo:[0,1] neg_hi:[0,1]
	v_pk_add_f32 v[34:35], v[44:45], v[34:35] op_sel_hi:[1,0] neg_lo:[0,1] neg_hi:[0,1]
	v_pk_mul_f32 v[36:37], v[132:133], v[36:37] op_sel_hi:[0,1]
	v_pk_mul_f32 v[34:35], v[132:133], v[34:35] op_sel_hi:[0,1]
	v_pk_fma_f32 v[36:37], v[112:113], v[36:37], v[120:121]
	v_pk_fma_f32 v[38:39], v[114:115], v[34:35], v[122:123]
	ds_write_b128 v57, v[36:39] offset:320
	v_pk_mul_f32 v[34:35], v[132:133], v[138:139] op_sel_hi:[0,1]
	v_pk_mul_f32 v[36:37], v[132:133], v[40:41] op_sel_hi:[0,1]
	s_waitcnt lgkmcnt(6)
	v_pk_fma_f32 v[34:35], v[104:105], v[34:35], v[128:129]
	v_pk_fma_f32 v[36:37], v[106:107], v[36:37], v[130:131]
	ds_write_b128 v57, v[34:37] offset:384
	v_pk_mul_f32 v[34:35], v[132:133], v[140:141] op_sel_hi:[0,1]
	v_pk_mul_f32 v[36:37], v[132:133], v[142:143] op_sel_hi:[0,1]
	v_pk_fma_f32 v[34:35], v[124:125], v[34:35], v[134:135]
	v_pk_fma_f32 v[36:37], v[126:127], v[36:37], v[136:137]
	v_add_u32_e32 v50, v83, v69
	ds_write_b128 v57, v[34:37] offset:448
	ds_read_b32 v84, v56 offset:8
	ds_read_b32 v85, v56 offset:16
	ds_read_b32 v86, v56 offset:24
	ds_read_b32 v87, v56 offset:32
	ds_read_b32 v88, v56 offset:40
	ds_read_b32 v89, v56 offset:48
	ds_read_b32 v90, v56 offset:56
	ds_read_b128 v[100:103], v50
	ds_read_b128 v[104:107], v81
	ds_read_b128 v[108:111], v80
	ds_read_b128 v[112:115], v80 offset:1088
	ds_read_b128 v[116:119], v80 offset:2176
	ds_read_b128 v[120:123], v80 offset:3264
	ds_read_b128 v[124:127], v80 offset:4352
	ds_read_b128 v[128:131], v80 offset:5440
	v_or_b32_e32 v51, 0x4400, v150
	s_mov_b32 s1, s0
	v_mov_b32_e32 v97, 0
	v_cmp_lt_i32_e32 vcc, -1, v68
	v_lshlrev_b32_e32 v96, 9, v68
	v_lshl_add_u64 v[92:93], v[0:1], 0, v[96:97]
	s_waitcnt lgkmcnt(7)
	s_and_saveexec_b64 s[2:3], vcc
	global_store_dwordx4 v[92:93], v[100:103], off nt
	s_mov_b64 exec, s[2:3]
	v_cmp_lt_i32_e32 vcc, -1, v84
	v_lshlrev_b32_e32 v96, 9, v84
	v_lshl_add_u64 v[94:95], v[0:1], 0, v[96:97]
	s_waitcnt lgkmcnt(6)
	s_and_saveexec_b64 s[2:3], vcc
	global_store_dwordx4 v[94:95], v[104:107], off nt
	s_mov_b64 exec, s[2:3]
	v_cmp_lt_i32_e32 vcc, -1, v85
	v_lshlrev_b32_e32 v96, 9, v85
	v_lshl_add_u64 v[92:93], v[0:1], 0, v[96:97]
	s_waitcnt lgkmcnt(5)
	s_and_saveexec_b64 s[2:3], vcc
	global_store_dwordx4 v[92:93], v[108:111], off nt
	s_mov_b64 exec, s[2:3]
	v_cmp_lt_i32_e32 vcc, -1, v86
	v_lshlrev_b32_e32 v96, 9, v86
	v_lshl_add_u64 v[94:95], v[0:1], 0, v[96:97]
	s_waitcnt lgkmcnt(4)
	s_and_saveexec_b64 s[2:3], vcc
	global_store_dwordx4 v[94:95], v[112:115], off nt
	s_mov_b64 exec, s[2:3]
	v_cmp_lt_i32_e32 vcc, -1, v87
	v_lshlrev_b32_e32 v96, 9, v87
	v_lshl_add_u64 v[92:93], v[0:1], 0, v[96:97]
	s_waitcnt lgkmcnt(3)
	s_and_saveexec_b64 s[2:3], vcc
	global_store_dwordx4 v[92:93], v[116:119], off nt
	s_mov_b64 exec, s[2:3]
	v_cmp_lt_i32_e32 vcc, -1, v88
	v_lshlrev_b32_e32 v96, 9, v88
	v_lshl_add_u64 v[94:95], v[0:1], 0, v[96:97]
	s_waitcnt lgkmcnt(2)
	s_and_saveexec_b64 s[2:3], vcc
	global_store_dwordx4 v[94:95], v[120:123], off nt
	s_mov_b64 exec, s[2:3]
	v_cmp_lt_i32_e32 vcc, -1, v89
	v_lshlrev_b32_e32 v96, 9, v89
	v_lshl_add_u64 v[92:93], v[0:1], 0, v[96:97]
	s_waitcnt lgkmcnt(1)
	s_and_saveexec_b64 s[2:3], vcc
	global_store_dwordx4 v[92:93], v[124:127], off nt
	s_mov_b64 exec, s[2:3]
	v_cmp_lt_i32_e32 vcc, -1, v90
	v_lshlrev_b32_e32 v96, 9, v90
	v_lshl_add_u64 v[94:95], v[0:1], 0, v[96:97]
	s_waitcnt lgkmcnt(0)
	s_and_saveexec_b64 s[2:3], vcc
	global_store_dwordx4 v[94:95], v[128:131], off nt
	s_mov_b64 exec, s[2:3]
.LBB2_117:
	s_or_b64 exec, exec, s[2:3]
	ds_read_b32 v36, v56 offset:64
	s_waitcnt lgkmcnt(0)
	v_cmp_lt_i32_e32 vcc, -1, v36
	s_and_saveexec_b64 s[2:3], vcc
	s_cbranch_execz .LBB2_134
	s_mov_b64 exec, s[2:3]
	ds_read2_b32 v[34:35], v56 offset0:16 offset1:18
	ds_read2_b32 v[46:47], v56 offset0:20 offset1:22
	ds_read2_b32 v[58:59], v56 offset0:24 offset1:26
	v_mov_b32_e32 v37, 0
	s_waitcnt lgkmcnt(3)
	v_max_i32_e32 v36, 0, v36
	v_lshlrev_b64 v[38:39], 9, v[36:37]
	s_waitcnt lgkmcnt(2)
	v_max_i32_e32 v36, 0, v35
	v_lshl_add_u64 v[48:49], v[66:67], 0, v[38:39]
	v_lshlrev_b64 v[38:39], 9, v[36:37]
	s_waitcnt lgkmcnt(1)
	v_max_i32_e32 v36, 0, v46
	v_lshl_add_u64 v[52:53], v[66:67], 0, v[38:39]
	global_load_dwordx4 v[38:41], v[48:49], off nt
	global_load_dwordx4 v[42:45], v[52:53], off nt
	v_lshlrev_b64 v[48:49], 9, v[36:37]
	v_max_i32_e32 v36, 0, v47
	v_lshl_add_u64 v[60:61], v[66:67], 0, v[48:49]
	v_lshlrev_b64 v[46:47], 9, v[36:37]
	v_lshl_add_u64 v[62:63], v[66:67], 0, v[46:47]
	global_load_dwordx4 v[46:49], v[60:61], off nt
	global_load_dwordx4 v[52:55], v[62:63], off nt
	ds_read2_b32 v[70:71], v56 offset0:28 offset1:30
	s_waitcnt lgkmcnt(1)
	v_max_i32_e32 v36, 0, v58
	v_lshlrev_b64 v[60:61], 9, v[36:37]
	v_max_i32_e32 v36, 0, v59
	v_lshl_add_u64 v[68:69], v[66:67], 0, v[60:61]
	v_lshlrev_b64 v[58:59], 9, v[36:37]
	s_waitcnt lgkmcnt(0)
	v_max_i32_e32 v36, 0, v70
	v_lshl_add_u64 v[72:73], v[66:67], 0, v[58:59]
	global_load_dwordx4 v[58:61], v[68:69], off nt
	global_load_dwordx4 v[62:65], v[72:73], off nt
	v_lshlrev_b64 v[68:69], 9, v[36:37]
	v_max_i32_e32 v36, 0, v71
	v_lshl_add_u64 v[74:75], v[66:67], 0, v[68:69]
	v_lshlrev_b64 v[68:69], 9, v[36:37]
	v_lshl_add_u64 v[76:77], v[66:67], 0, v[68:69]
	global_load_dwordx4 v[66:69], v[74:75], off nt
	global_load_dwordx4 v[70:73], v[76:77], off nt
	s_waitcnt vmcnt(7)
	ds_write_b128 v50, v[38:41]
	s_waitcnt vmcnt(6)
	ds_write_b128 v50, v[42:45] offset:1088
	s_waitcnt vmcnt(5)
	ds_write_b128 v50, v[46:49] offset:2176
	s_waitcnt vmcnt(4)
	ds_write_b128 v50, v[52:55] offset:3264
	s_waitcnt vmcnt(3)
	ds_write_b128 v50, v[58:61] offset:4352
	s_waitcnt vmcnt(2)
	ds_write_b128 v50, v[62:65] offset:5440
	s_waitcnt vmcnt(1)
	ds_write_b128 v50, v[66:69] offset:6528
	s_waitcnt vmcnt(0)
	ds_write_b128 v50, v[70:73] offset:7616
	ds_read_b128 v[38:41], v82
	ds_read_b128 v[52:55], v82 offset:64
	ds_read_b128 v[58:61], v82 offset:128
	ds_read_b128 v[62:65], v82 offset:192
	ds_read_b128 v[66:69], v82 offset:256
	ds_read_b128 v[70:73], v82 offset:320
	ds_read_b128 v[74:77], v82 offset:384
	ds_read_b128 v[82:85], v82 offset:448
	s_waitcnt lgkmcnt(7)
	v_pk_fma_f32 v[48:49], s[0:1], v[6:7], v[38:39]
	v_pk_fma_f32 v[46:47], s[0:1], v[8:9], v[40:41]
	s_waitcnt lgkmcnt(6)
	v_pk_fma_f32 v[44:45], s[0:1], v[10:11], v[52:53]
	v_pk_fma_f32 v[42:43], s[0:1], v[12:13], v[54:55]
	s_waitcnt lgkmcnt(5)
	v_pk_fma_f32 v[40:41], s[0:1], v[14:15], v[58:59]
	v_pk_fma_f32 v[38:39], s[0:1], v[16:17], v[60:61]
	s_waitcnt lgkmcnt(4)
	v_pk_fma_f32 v[16:17], s[0:1], v[18:19], v[62:63]
	v_pk_fma_f32 v[14:15], s[0:1], v[20:21], v[64:65]
	s_waitcnt lgkmcnt(3)
	v_pk_fma_f32 v[12:13], s[0:1], v[22:23], v[66:67]
	s_waitcnt lgkmcnt(0)
	v_pk_fma_f32 v[58:59], s[0:1], v[2:3], v[82:83]
	v_mov_b32_e32 v2, v48
	v_mov_b32_e32 v3, v44
	v_mov_b32_e32 v18, v49
	v_mov_b32_e32 v19, v45
	v_mov_b32_e32 v20, v46
	v_mov_b32_e32 v21, v42
	v_mov_b32_e32 v22, v47
	v_mov_b32_e32 v23, v43
	v_pk_fma_f32 v[10:11], s[0:1], v[24:25], v[68:69]
	v_pk_fma_f32 v[8:9], s[0:1], v[26:27], v[70:71]
	v_mov_b32_e32 v24, v40
	v_mov_b32_e32 v25, v38
	v_mov_b32_e32 v26, v41
	v_mov_b32_e32 v27, v39
	v_pk_add_f32 v[2:3], v[2:3], v[18:19]
	v_pk_add_f32 v[18:19], v[20:21], v[22:23]
	v_pk_add_f32 v[20:21], v[24:25], v[26:27]
	v_pk_add_f32 v[2:3], v[2:3], v[18:19]
	v_pk_fma_f32 v[6:7], s[0:1], v[28:29], v[72:73]
	v_pk_fma_f32 v[52:53], s[0:1], v[30:31], v[74:75]
	v_pk_add_f32 v[28:29], v[16:17], v[16:17] op_sel:[0,1] op_sel_hi:[1,0]
	v_pk_add_f32 v[30:31], v[14:15], v[14:15] op_sel:[0,1] op_sel_hi:[1,0]
	v_pk_add_f32 v[18:19], v[20:21], v[20:21] op_sel:[0,1] op_sel_hi:[1,0]
	v_add_f32_e32 v2, 0, v2
	v_pk_fma_f32 v[54:55], s[0:1], v[32:33], v[76:77]
	v_mov_b32_e32 v33, v12
	v_mov_b32_e32 v29, v10
	v_mov_b32_e32 v31, v11
	v_mov_b32_e32 v19, v13
	v_add_f32_e32 v32, v2, v3
	v_mov_b32_e32 v60, v8
	v_mov_b32_e32 v61, v6
	v_mov_b32_e32 v62, v9
	v_mov_b32_e32 v63, v7
	v_pk_add_f32 v[20:21], v[28:29], v[30:31]
	v_pk_add_f32 v[2:3], v[32:33], v[18:19]
	v_pk_add_f32 v[22:23], v[60:61], v[62:63]
	v_pk_add_f32 v[2:3], v[2:3], v[20:21]
	v_pk_fma_f32 v[4:5], s[0:1], v[4:5], v[84:85]
	v_pk_add_f32 v[64:65], v[52:53], v[52:53] op_sel:[0,1] op_sel_hi:[1,0]
	v_pk_add_f32 v[66:67], v[54:55], v[54:55] op_sel:[0,1] op_sel_hi:[1,0]
	v_pk_add_f32 v[22:23], v[22:23], v[22:23] op_sel:[0,1] op_sel_hi:[1,0]
	v_pk_add_f32 v[2:3], v[2:3], v[2:3] op_sel:[0,1] op_sel_hi:[1,0]
	v_mov_b32_e32 v65, v4
	v_mov_b32_e32 v67, v5
	v_mov_b32_e32 v23, v59
	v_mov_b32_e32 v3, v58
	v_pk_add_f32 v[2:3], v[2:3], v[22:23]
	v_pk_add_f32 v[18:19], v[64:65], v[66:67]
	s_mov_b32 s0, 0x800000
	v_pk_add_f32 v[2:3], v[2:3], v[18:19]
	ds_read_b128 v[18:21], v51 offset:2048
	ds_read_b128 v[22:25], v51 offset:2112
	ds_read_b128 v[26:29], v51 offset:2560
	ds_read_b128 v[30:33], v51 offset:2624
	v_add_f32_e32 v2, v2, v3
	ds_bpermute_b32 v3, v149, v2
	s_waitcnt lgkmcnt(0)
	v_add_f32_e32 v2, v2, v3
	ds_bpermute_b32 v3, v148, v2
	s_waitcnt lgkmcnt(0)
	v_add_f32_e32 v3, v2, v3
	v_fmamk_f32 v36, v3, 0xbc000000, v49
	v_fmamk_f32 v35, v3, 0xbc000000, v48
	v_mul_f32_e32 v36, v36, v36
	v_fmamk_f32 v60, v3, 0xbc000000, v46
	v_fmac_f32_e32 v36, v35, v35
	v_fmac_f32_e32 v36, v60, v60
	v_fmamk_f32 v35, v3, 0xbc000000, v47
	v_fmac_f32_e32 v36, v35, v35
	v_fmamk_f32 v35, v3, 0xbc000000, v44
	v_fmac_f32_e32 v36, v35, v35
	v_fmamk_f32 v35, v3, 0xbc000000, v45
	v_fmac_f32_e32 v36, v35, v35
	v_fmamk_f32 v35, v3, 0xbc000000, v42
	v_fmac_f32_e32 v36, v35, v35
	v_fmamk_f32 v35, v3, 0xbc000000, v43
	v_fmac_f32_e32 v36, v35, v35
	v_fmamk_f32 v35, v3, 0xbc000000, v40
	v_fmac_f32_e32 v36, v35, v35
	v_fmamk_f32 v35, v3, 0xbc000000, v41
	v_fmac_f32_e32 v36, v35, v35
	v_fmamk_f32 v35, v3, 0xbc000000, v38
	v_fmac_f32_e32 v36, v35, v35
	v_fmamk_f32 v35, v3, 0xbc000000, v39
	v_fmac_f32_e32 v36, v35, v35
	v_fmamk_f32 v35, v3, 0xbc000000, v16
	v_fmac_f32_e32 v36, v35, v35
	v_fmamk_f32 v35, v3, 0xbc000000, v17
	v_fmac_f32_e32 v36, v35, v35
	v_fmamk_f32 v35, v3, 0xbc000000, v14
	v_fmac_f32_e32 v36, v35, v35
	v_fmamk_f32 v35, v3, 0xbc000000, v15
	v_fmac_f32_e32 v36, v35, v35
	v_fmamk_f32 v35, v3, 0xbc000000, v12
	v_fmac_f32_e32 v36, v35, v35
	v_fmamk_f32 v35, v3, 0xbc000000, v13
	v_fmac_f32_e32 v36, v35, v35
	v_fmamk_f32 v35, v3, 0xbc000000, v10
	v_fmac_f32_e32 v36, v35, v35
	v_fmamk_f32 v35, v3, 0xbc000000, v11
	v_fmac_f32_e32 v36, v35, v35
	v_fmamk_f32 v35, v3, 0xbc000000, v8
	v_fmac_f32_e32 v36, v35, v35
	v_fmamk_f32 v35, v3, 0xbc000000, v9
	v_mul_f32_e32 v2, 0x3c000000, v3
	v_fmac_f32_e32 v36, v35, v35
	v_fmamk_f32 v35, v3, 0xbc000000, v6
	v_fmamk_f32 v3, v3, 0xbc000000, v7
	v_fmac_f32_e32 v36, v35, v35
	v_pk_add_f32 v[78:79], v[52:53], v[2:3] op_sel_hi:[1,0] neg_lo:[0,1] neg_hi:[0,1]
	v_fmac_f32_e32 v36, v3, v3
	v_pk_mul_f32 v[52:53], v[78:79], v[78:79]
	s_nop 0
	v_add_f32_e32 v3, v52, v36
	v_add_f32_e32 v3, v53, v3
	v_pk_add_f32 v[106:107], v[54:55], v[2:3] op_sel_hi:[1,0] neg_lo:[0,1] neg_hi:[0,1]
	s_nop 0
	v_pk_mul_f32 v[52:53], v[106:107], v[106:107]
	s_nop 0
	v_add_f32_e32 v3, v52, v3
	v_add_f32_e32 v3, v53, v3
	v_pk_add_f32 v[108:109], v[58:59], v[2:3] op_sel_hi:[1,0] neg_lo:[0,1] neg_hi:[0,1]
	s_nop 0
	v_pk_mul_f32 v[52:53], v[108:109], v[108:109]
	s_nop 0
	v_add_f32_e32 v3, v52, v3
	v_add_f32_e32 v3, v53, v3
	v_pk_add_f32 v[110:111], v[4:5], v[2:3] op_sel_hi:[1,0] neg_lo:[0,1] neg_hi:[0,1]
	ds_read_b128 v[52:55], v51 offset:2176
	ds_read_b128 v[58:61], v51 offset:2240
	ds_read_b128 v[62:65], v51 offset:2688
	ds_read_b128 v[66:69], v51 offset:2752
	v_pk_mul_f32 v[4:5], v[110:111], v[110:111]
	ds_read_b128 v[70:73], v51 offset:2304
	ds_read_b128 v[74:77], v51 offset:2368
	ds_read_b128 v[82:85], v51 offset:2816
	ds_read_b128 v[86:89], v51 offset:2880
	v_add_f32_e32 v3, v4, v3
	v_add_f32_e32 v3, v5, v3
	ds_bpermute_b32 v4, v149, v3
	ds_read_b128 v[90:93], v51 offset:2432
	ds_read_b128 v[94:97], v51 offset:2496
	ds_read_b128 v[98:101], v51 offset:2944
	ds_read_b128 v[102:105], v51 offset:3008
	s_waitcnt lgkmcnt(4)
	v_add_f32_e32 v3, v3, v4
	ds_bpermute_b32 v4, v148, v3
	s_waitcnt lgkmcnt(0)
	v_add_f32_e32 v3, v3, v4
	v_mov_b32_e32 v4, 0x3727c5ac
	v_fmac_f32_e32 v4, 0x3c000000, v3
	v_mul_f32_e32 v3, 0x4b800000, v4
	v_cmp_gt_f32_e32 vcc, s0, v4
	s_nop 1
	v_cndmask_b32_e32 v3, v4, v3, vcc
	v_rsq_f32_e32 v3, v3
	s_nop 0
	v_mul_f32_e32 v4, 0x45800000, v3
	v_cndmask_b32_e32 v36, v3, v4, vcc
	v_pk_add_f32 v[4:5], v[48:49], v[2:3] op_sel_hi:[1,0] neg_lo:[0,1] neg_hi:[0,1]
	v_cmp_lt_i32_e32 vcc, -1, v34
	v_pk_mul_f32 v[4:5], v[36:37], v[4:5] op_sel_hi:[0,1]
	v_pk_fma_f32 v[18:19], v[18:19], v[4:5], v[26:27]
	v_pk_add_f32 v[4:5], v[46:47], v[2:3] op_sel_hi:[1,0] neg_lo:[0,1] neg_hi:[0,1]
	s_nop 0
	v_pk_mul_f32 v[4:5], v[36:37], v[4:5] op_sel_hi:[0,1]
	v_pk_fma_f32 v[20:21], v[20:21], v[4:5], v[28:29]
	v_pk_add_f32 v[4:5], v[44:45], v[2:3] op_sel_hi:[1,0] neg_lo:[0,1] neg_hi:[0,1]
	ds_write_b128 v57, v[18:21]
	v_pk_mul_f32 v[4:5], v[36:37], v[4:5] op_sel_hi:[0,1]
	v_pk_fma_f32 v[18:19], v[22:23], v[4:5], v[30:31]
	v_pk_add_f32 v[4:5], v[42:43], v[2:3] op_sel_hi:[1,0] neg_lo:[0,1] neg_hi:[0,1]
	s_nop 0
	v_pk_mul_f32 v[4:5], v[36:37], v[4:5] op_sel_hi:[0,1]
	v_pk_fma_f32 v[20:21], v[24:25], v[4:5], v[32:33]
	v_pk_add_f32 v[4:5], v[40:41], v[2:3] op_sel_hi:[1,0] neg_lo:[0,1] neg_hi:[0,1]
	ds_write_b128 v57, v[18:21] offset:64
	v_pk_mul_f32 v[4:5], v[36:37], v[4:5] op_sel_hi:[0,1]
	v_pk_fma_f32 v[18:19], v[52:53], v[4:5], v[62:63]
	v_pk_add_f32 v[4:5], v[38:39], v[2:3] op_sel_hi:[1,0] neg_lo:[0,1] neg_hi:[0,1]
	s_nop 0
	v_pk_mul_f32 v[4:5], v[36:37], v[4:5] op_sel_hi:[0,1]
	v_pk_fma_f32 v[20:21], v[54:55], v[4:5], v[64:65]
	v_pk_add_f32 v[4:5], v[16:17], v[2:3] op_sel_hi:[1,0] neg_lo:[0,1] neg_hi:[0,1]
	ds_write_b128 v57, v[18:21] offset:128
	v_pk_mul_f32 v[4:5], v[36:37], v[4:5] op_sel_hi:[0,1]
	v_pk_fma_f32 v[16:17], v[58:59], v[4:5], v[66:67]
	v_pk_add_f32 v[4:5], v[14:15], v[2:3] op_sel_hi:[1,0] neg_lo:[0,1] neg_hi:[0,1]
	s_nop 0
	v_pk_mul_f32 v[4:5], v[36:37], v[4:5] op_sel_hi:[0,1]
	v_pk_fma_f32 v[18:19], v[60:61], v[4:5], v[68:69]
	v_pk_add_f32 v[4:5], v[12:13], v[2:3] op_sel_hi:[1,0] neg_lo:[0,1] neg_hi:[0,1]
	ds_write_b128 v57, v[16:19] offset:192
	v_pk_mul_f32 v[4:5], v[36:37], v[4:5] op_sel_hi:[0,1]
	v_pk_fma_f32 v[12:13], v[70:71], v[4:5], v[82:83]
	v_pk_add_f32 v[4:5], v[10:11], v[2:3] op_sel_hi:[1,0] neg_lo:[0,1] neg_hi:[0,1]
	s_nop 0
	v_pk_mul_f32 v[4:5], v[36:37], v[4:5] op_sel_hi:[0,1]
	v_pk_fma_f32 v[14:15], v[72:73], v[4:5], v[84:85]
	v_pk_add_f32 v[4:5], v[8:9], v[2:3] op_sel_hi:[1,0] neg_lo:[0,1] neg_hi:[0,1]
	v_pk_add_f32 v[2:3], v[6:7], v[2:3] op_sel_hi:[1,0] neg_lo:[0,1] neg_hi:[0,1]
	v_pk_mul_f32 v[4:5], v[36:37], v[4:5] op_sel_hi:[0,1]
	v_pk_mul_f32 v[2:3], v[36:37], v[2:3] op_sel_hi:[0,1]
	v_pk_fma_f32 v[4:5], v[74:75], v[4:5], v[86:87]
	v_pk_fma_f32 v[6:7], v[76:77], v[2:3], v[88:89]
	ds_write_b128 v57, v[4:7] offset:320
	v_pk_mul_f32 v[2:3], v[36:37], v[78:79] op_sel_hi:[0,1]
	v_pk_mul_f32 v[4:5], v[36:37], v[106:107] op_sel_hi:[0,1]
	v_pk_fma_f32 v[2:3], v[90:91], v[2:3], v[98:99]
	v_pk_fma_f32 v[4:5], v[92:93], v[4:5], v[100:101]
	ds_write_b128 v57, v[2:5] offset:384
	v_pk_mul_f32 v[2:3], v[36:37], v[108:109] op_sel_hi:[0,1]
	v_pk_mul_f32 v[4:5], v[36:37], v[110:111] op_sel_hi:[0,1]
	v_pk_fma_f32 v[2:3], v[94:95], v[2:3], v[102:103]
	v_pk_fma_f32 v[4:5], v[96:97], v[4:5], v[104:105]
	ds_write_b128 v57, v[12:15] offset:256
	ds_write_b128 v57, v[2:5] offset:448
	ds_read_b32 v84, v56 offset:72
	ds_read_b32 v85, v56 offset:80
	ds_read_b32 v86, v56 offset:88
	ds_read_b32 v87, v56 offset:96
	ds_read_b32 v88, v56 offset:104
	ds_read_b32 v89, v56 offset:112
	ds_read_b32 v90, v56 offset:120
	ds_read_b128 v[100:103], v50
	ds_read_b128 v[104:107], v81
	ds_read_b128 v[108:111], v80
	ds_read_b128 v[112:115], v80 offset:1088
	ds_read_b128 v[116:119], v80 offset:2176
	ds_read_b128 v[120:123], v80 offset:3264
	ds_read_b128 v[124:127], v80 offset:4352
	ds_read_b128 v[128:131], v80 offset:5440
	v_mov_b32_e32 v97, 0
	v_cmp_lt_i32_e32 vcc, -1, v34
	v_lshlrev_b32_e32 v96, 9, v34
	v_lshl_add_u64 v[92:93], v[0:1], 0, v[96:97]
	s_waitcnt lgkmcnt(7)
	s_and_saveexec_b64 s[0:1], vcc
	global_store_dwordx4 v[92:93], v[100:103], off nt
	s_mov_b64 exec, s[0:1]
	v_cmp_lt_i32_e32 vcc, -1, v84
	v_lshlrev_b32_e32 v96, 9, v84
	v_lshl_add_u64 v[94:95], v[0:1], 0, v[96:97]
	s_waitcnt lgkmcnt(6)
	s_and_saveexec_b64 s[0:1], vcc
	global_store_dwordx4 v[94:95], v[104:107], off nt
	s_mov_b64 exec, s[0:1]
	v_cmp_lt_i32_e32 vcc, -1, v85
	v_lshlrev_b32_e32 v96, 9, v85
	v_lshl_add_u64 v[92:93], v[0:1], 0, v[96:97]
	s_waitcnt lgkmcnt(5)
	s_and_saveexec_b64 s[0:1], vcc
	global_store_dwordx4 v[92:93], v[108:111], off nt
	s_mov_b64 exec, s[0:1]
	v_cmp_lt_i32_e32 vcc, -1, v86
	v_lshlrev_b32_e32 v96, 9, v86
	v_lshl_add_u64 v[94:95], v[0:1], 0, v[96:97]
	s_waitcnt lgkmcnt(4)
	s_and_saveexec_b64 s[0:1], vcc
	global_store_dwordx4 v[94:95], v[112:115], off nt
	s_mov_b64 exec, s[0:1]
	v_cmp_lt_i32_e32 vcc, -1, v87
	v_lshlrev_b32_e32 v96, 9, v87
	v_lshl_add_u64 v[92:93], v[0:1], 0, v[96:97]
	s_waitcnt lgkmcnt(3)
	s_and_saveexec_b64 s[0:1], vcc
	global_store_dwordx4 v[92:93], v[116:119], off nt
	s_mov_b64 exec, s[0:1]
	v_cmp_lt_i32_e32 vcc, -1, v88
	v_lshlrev_b32_e32 v96, 9, v88
	v_lshl_add_u64 v[94:95], v[0:1], 0, v[96:97]
	s_waitcnt lgkmcnt(2)
	s_and_saveexec_b64 s[0:1], vcc
	global_store_dwordx4 v[94:95], v[120:123], off nt
	s_mov_b64 exec, s[0:1]
	v_cmp_lt_i32_e32 vcc, -1, v89
	v_lshlrev_b32_e32 v96, 9, v89
	v_lshl_add_u64 v[92:93], v[0:1], 0, v[96:97]
	s_waitcnt lgkmcnt(1)
	s_and_saveexec_b64 s[0:1], vcc
	global_store_dwordx4 v[92:93], v[124:127], off nt
	s_mov_b64 exec, s[0:1]
	v_cmp_lt_i32_e32 vcc, -1, v90
	v_lshlrev_b32_e32 v96, 9, v90
	v_lshl_add_u64 v[94:95], v[0:1], 0, v[96:97]
	s_waitcnt lgkmcnt(0)
	s_and_saveexec_b64 s[0:1], vcc
	global_store_dwordx4 v[94:95], v[128:131], off nt
	s_mov_b64 exec, s[0:1]
